# GEMM K-loops: per-segment s_setprio toggles removed (priority left to age-based arbitration), on top of v34
# baseline (speedup 1.0000x reference)
.LBB0_290:
	s_add_u32 s46, s44, 0xfffc0080
	s_addc_u32 s47, s45, -1
	s_add_i32 s62, 0, 0x10000
	s_cmp_eq_u32 s61, 12
	s_cselect_b32 s49, s1, s47
	s_cselect_b32 s48, s5, s46
	s_cselect_b32 s47, s35, s60
	s_cselect_b32 s46, s37, s59
	s_add_i32 s64, 0, 0x14000
	v_add_u32_e32 v158, s62, v148
	v_add_u32_e32 v174, s64, v148
	ds_read_b128 v[144:147], v158
	ds_read_b128 v[150:153], v158 offset:1024
	ds_read_b128 v[154:157], v158 offset:2048
	ds_read_b128 v[158:161], v158 offset:3072
	ds_read_b128 v[162:165], v174
	ds_read_b128 v[166:169], v174 offset:1024
	ds_read_b128 v[170:173], v174 offset:2048
	ds_read_b128 v[174:177], v174 offset:3072
	v_lshl_add_u64 v[210:211], s[44:45], 0, v[140:141]
	s_add_i32 m0, s50, 0xc000
	ds_read_b128 v[178:181], v149
	ds_read_b128 v[182:185], v149 offset:1024
	ds_read_b128 v[186:189], v149 offset:2048
	ds_read_b128 v[190:193], v149 offset:3072
	ds_read_b128 v[194:197], v149 offset:4096
	ds_read_b128 v[198:201], v149 offset:5120
	ds_read_b128 v[202:205], v149 offset:6144
	ds_read_b128 v[206:209], v149 offset:7168
	global_load_lds_dwordx4 v[210:211], off
	v_lshl_add_u64 v[210:211], s[44:45], 0, v[142:143]
	s_add_i32 m0, s50, 0xe000
	s_nop 0
	global_load_lds_dwordx4 v[210:211], off
	s_waitcnt vmcnt(8)
	s_waitcnt lgkmcnt(0)
	s_barrier
	s_waitcnt lgkmcnt(0)
	v_mfma_f32_16x16x32_bf16 v[130:133], v[144:147], v[178:181], v[130:133]
	v_mfma_f32_16x16x32_bf16 v[126:129], v[154:157], v[178:181], v[126:129]
	v_mfma_f32_16x16x32_bf16 v[114:117], v[144:147], v[186:189], v[114:117]
	v_mfma_f32_16x16x32_bf16 v[110:113], v[154:157], v[186:189], v[110:113]
	v_mfma_f32_16x16x32_bf16 v[98:101], v[144:147], v[194:197], v[98:101]
	v_mfma_f32_16x16x32_bf16 v[94:97], v[154:157], v[194:197], v[94:97]
	v_mfma_f32_16x16x32_bf16 v[82:85], v[144:147], v[202:205], v[82:85]
	v_mfma_f32_16x16x32_bf16 v[78:81], v[154:157], v[202:205], v[78:81]
	v_mfma_f32_16x16x32_bf16 v[130:133], v[150:153], v[182:185], v[130:133]
	v_mfma_f32_16x16x32_bf16 v[126:129], v[158:161], v[182:185], v[126:129]
	v_mfma_f32_16x16x32_bf16 v[114:117], v[150:153], v[190:193], v[114:117]
	v_mfma_f32_16x16x32_bf16 v[110:113], v[158:161], v[190:193], v[110:113]
	v_mfma_f32_16x16x32_bf16 v[98:101], v[150:153], v[198:201], v[98:101]
	v_mfma_f32_16x16x32_bf16 v[94:97], v[158:161], v[198:201], v[94:97]
	v_mfma_f32_16x16x32_bf16 v[82:85], v[150:153], v[206:209], v[82:85]
	v_mfma_f32_16x16x32_bf16 v[78:81], v[158:161], v[206:209], v[78:81]
	v_mfma_f32_16x16x32_bf16 v[122:125], v[162:165], v[178:181], v[122:125]
	v_mfma_f32_16x16x32_bf16 v[118:121], v[170:173], v[178:181], v[118:121]
	v_mfma_f32_16x16x32_bf16 v[106:109], v[162:165], v[186:189], v[106:109]
	v_mfma_f32_16x16x32_bf16 v[102:105], v[170:173], v[186:189], v[102:105]
	v_mfma_f32_16x16x32_bf16 v[90:93], v[162:165], v[194:197], v[90:93]
	v_mfma_f32_16x16x32_bf16 v[86:89], v[170:173], v[194:197], v[86:89]
	v_mfma_f32_16x16x32_bf16 v[74:77], v[162:165], v[202:205], v[74:77]
	v_mfma_f32_16x16x32_bf16 v[70:73], v[170:173], v[202:205], v[70:73]
	v_mfma_f32_16x16x32_bf16 v[122:125], v[166:169], v[182:185], v[122:125]
	v_mfma_f32_16x16x32_bf16 v[118:121], v[174:177], v[182:185], v[118:121]
	v_mfma_f32_16x16x32_bf16 v[106:109], v[166:169], v[190:193], v[106:109]
	v_mfma_f32_16x16x32_bf16 v[102:105], v[174:177], v[190:193], v[102:105]
	v_mfma_f32_16x16x32_bf16 v[90:93], v[166:169], v[198:201], v[90:93]
	v_mfma_f32_16x16x32_bf16 v[86:89], v[174:177], v[198:201], v[86:89]
	v_mfma_f32_16x16x32_bf16 v[74:77], v[166:169], v[206:209], v[74:77]
	v_mfma_f32_16x16x32_bf16 v[70:73], v[174:177], v[206:209], v[70:73]
	s_barrier
	s_add_i32 s62, s62, s27
	v_lshl_add_u64 v[210:211], s[46:47], 0, v[0:1]
	s_mov_b32 m0, s62
	ds_read_b128 v[178:181], v149 offset:16384
	ds_read_b128 v[182:185], v149 offset:17408
	ds_read_b128 v[186:189], v149 offset:18432
	ds_read_b128 v[190:193], v149 offset:19456
	ds_read_b128 v[194:197], v149 offset:20480
	ds_read_b128 v[198:201], v149 offset:21504
	ds_read_b128 v[202:205], v149 offset:22528
	ds_read_b128 v[206:209], v149 offset:23552
	global_load_lds_dwordx4 v[210:211], off
	s_add_i32 m0, s62, 0x2000
	s_add_u32 s62, s46, 0x40000
	v_lshl_add_u64 v[212:213], s[46:47], 0, v[138:139]
	s_addc_u32 s63, s47, 0
	s_add_i32 s64, s64, s27
	global_load_lds_dwordx4 v[212:213], off
	v_lshl_add_u64 v[216:217], s[62:63], 0, v[0:1]
	s_mov_b32 m0, s64
	v_lshl_add_u64 v[218:219], s[48:49], 0, v[136:137]
	global_load_lds_dwordx4 v[216:217], off
	v_lshl_add_u64 v[216:217], s[62:63], 0, v[138:139]
	s_add_i32 m0, s64, 0x2000
	s_nop 0
	global_load_lds_dwordx4 v[216:217], off
	v_lshl_add_u64 v[216:217], s[48:49], 0, v[134:135]
	s_mov_b32 m0, s50
	s_nop 0
	global_load_lds_dwordx4 v[216:217], off
	s_mov_b32 m0, s51
	s_nop 0
	global_load_lds_dwordx4 v[218:219], off
	s_waitcnt vmcnt(8)
	s_waitcnt lgkmcnt(0)
	s_barrier
	s_waitcnt lgkmcnt(0)
	v_mfma_f32_16x16x32_bf16 v[66:69], v[144:147], v[178:181], v[66:69]
	v_mfma_f32_16x16x32_bf16 v[62:65], v[154:157], v[178:181], v[62:65]
	v_mfma_f32_16x16x32_bf16 v[50:53], v[144:147], v[186:189], v[50:53]
	v_mfma_f32_16x16x32_bf16 v[46:49], v[154:157], v[186:189], v[46:49]
	v_mfma_f32_16x16x32_bf16 v[34:37], v[144:147], v[194:197], v[34:37]
	v_mfma_f32_16x16x32_bf16 v[30:33], v[154:157], v[194:197], v[30:33]
	v_mfma_f32_16x16x32_bf16 v[18:21], v[144:147], v[202:205], v[18:21]
	v_mfma_f32_16x16x32_bf16 v[14:17], v[154:157], v[202:205], v[14:17]
	v_mfma_f32_16x16x32_bf16 v[66:69], v[150:153], v[182:185], v[66:69]
	v_mfma_f32_16x16x32_bf16 v[62:65], v[158:161], v[182:185], v[62:65]
	v_mfma_f32_16x16x32_bf16 v[50:53], v[150:153], v[190:193], v[50:53]
	v_mfma_f32_16x16x32_bf16 v[46:49], v[158:161], v[190:193], v[46:49]
	v_mfma_f32_16x16x32_bf16 v[34:37], v[150:153], v[198:201], v[34:37]
	v_mfma_f32_16x16x32_bf16 v[30:33], v[158:161], v[198:201], v[30:33]
	v_mfma_f32_16x16x32_bf16 v[18:21], v[150:153], v[206:209], v[18:21]
	v_mfma_f32_16x16x32_bf16 v[14:17], v[158:161], v[206:209], v[14:17]
	v_mfma_f32_16x16x32_bf16 v[58:61], v[162:165], v[178:181], v[58:61]
	v_mfma_f32_16x16x32_bf16 v[54:57], v[170:173], v[178:181], v[54:57]
	v_mfma_f32_16x16x32_bf16 v[42:45], v[162:165], v[186:189], v[42:45]
	v_mfma_f32_16x16x32_bf16 v[38:41], v[170:173], v[186:189], v[38:41]
	v_mfma_f32_16x16x32_bf16 v[26:29], v[162:165], v[194:197], v[26:29]
	v_mfma_f32_16x16x32_bf16 v[22:25], v[170:173], v[194:197], v[22:25]
	v_mfma_f32_16x16x32_bf16 v[10:13], v[162:165], v[202:205], v[10:13]
	v_mfma_f32_16x16x32_bf16 v[6:9], v[170:173], v[202:205], v[6:9]
	v_mfma_f32_16x16x32_bf16 v[58:61], v[166:169], v[182:185], v[58:61]
	v_mfma_f32_16x16x32_bf16 v[54:57], v[174:177], v[182:185], v[54:57]
	v_mfma_f32_16x16x32_bf16 v[42:45], v[166:169], v[190:193], v[42:45]
	v_mfma_f32_16x16x32_bf16 v[38:41], v[174:177], v[190:193], v[38:41]
	v_mfma_f32_16x16x32_bf16 v[26:29], v[166:169], v[198:201], v[26:29]
	v_mfma_f32_16x16x32_bf16 v[22:25], v[174:177], v[198:201], v[22:25]
	v_mfma_f32_16x16x32_bf16 v[10:13], v[166:169], v[206:209], v[10:13]
	v_mfma_f32_16x16x32_bf16 v[6:9], v[174:177], v[206:209], v[6:9]
	s_barrier
	s_add_i32 s62, 0, 0x18000
	s_add_i32 s63, 0, 0x1c000
	v_add_u32_e32 v158, s62, v148
	v_add_u32_e32 v174, s63, v148
	ds_read_b128 v[144:147], v158
	ds_read_b128 v[150:153], v158 offset:1024
	ds_read_b128 v[154:157], v158 offset:2048
	ds_read_b128 v[158:161], v158 offset:3072
	ds_read_b128 v[162:165], v174
	ds_read_b128 v[166:169], v174 offset:1024
	ds_read_b128 v[170:173], v174 offset:2048
	ds_read_b128 v[174:177], v174 offset:3072
	s_add_u32 s48, s48, 0x40000
	s_addc_u32 s49, s49, 0
	s_mov_b32 m0, s52
	v_lshl_add_u64 v[220:221], s[48:49], 0, v[134:135]
	ds_read_b128 v[178:181], v149 offset:32768
	ds_read_b128 v[182:185], v149 offset:33792
	ds_read_b128 v[186:189], v149 offset:34816
	ds_read_b128 v[190:193], v149 offset:35840
	ds_read_b128 v[194:197], v149 offset:36864
	ds_read_b128 v[198:201], v149 offset:37888
	ds_read_b128 v[202:205], v149 offset:38912
	ds_read_b128 v[206:209], v149 offset:39936
	global_load_lds_dwordx4 v[220:221], off
	v_lshl_add_u64 v[220:221], s[48:49], 0, v[136:137]
	s_mov_b32 m0, s53
	s_nop 0
	global_load_lds_dwordx4 v[220:221], off
	s_waitcnt vmcnt(8)
	s_waitcnt lgkmcnt(0)
	s_barrier
	s_waitcnt lgkmcnt(0)
	v_mfma_f32_16x16x32_bf16 v[130:133], v[144:147], v[178:181], v[130:133]
	v_mfma_f32_16x16x32_bf16 v[126:129], v[154:157], v[178:181], v[126:129]
	v_mfma_f32_16x16x32_bf16 v[114:117], v[144:147], v[186:189], v[114:117]
	v_mfma_f32_16x16x32_bf16 v[110:113], v[154:157], v[186:189], v[110:113]
	v_mfma_f32_16x16x32_bf16 v[98:101], v[144:147], v[194:197], v[98:101]
	v_mfma_f32_16x16x32_bf16 v[94:97], v[154:157], v[194:197], v[94:97]
	v_mfma_f32_16x16x32_bf16 v[82:85], v[144:147], v[202:205], v[82:85]
	v_mfma_f32_16x16x32_bf16 v[78:81], v[154:157], v[202:205], v[78:81]
	v_mfma_f32_16x16x32_bf16 v[130:133], v[150:153], v[182:185], v[130:133]
	v_mfma_f32_16x16x32_bf16 v[126:129], v[158:161], v[182:185], v[126:129]
	v_mfma_f32_16x16x32_bf16 v[114:117], v[150:153], v[190:193], v[114:117]
	v_mfma_f32_16x16x32_bf16 v[110:113], v[158:161], v[190:193], v[110:113]
	v_mfma_f32_16x16x32_bf16 v[98:101], v[150:153], v[198:201], v[98:101]
	v_mfma_f32_16x16x32_bf16 v[94:97], v[158:161], v[198:201], v[94:97]
	v_mfma_f32_16x16x32_bf16 v[82:85], v[150:153], v[206:209], v[82:85]
	v_mfma_f32_16x16x32_bf16 v[78:81], v[158:161], v[206:209], v[78:81]
	v_mfma_f32_16x16x32_bf16 v[122:125], v[162:165], v[178:181], v[122:125]
	v_mfma_f32_16x16x32_bf16 v[118:121], v[170:173], v[178:181], v[118:121]
	v_mfma_f32_16x16x32_bf16 v[106:109], v[162:165], v[186:189], v[106:109]
	v_mfma_f32_16x16x32_bf16 v[102:105], v[170:173], v[186:189], v[102:105]
	v_mfma_f32_16x16x32_bf16 v[90:93], v[162:165], v[194:197], v[90:93]
	v_mfma_f32_16x16x32_bf16 v[86:89], v[170:173], v[194:197], v[86:89]
	v_mfma_f32_16x16x32_bf16 v[74:77], v[162:165], v[202:205], v[74:77]
	v_mfma_f32_16x16x32_bf16 v[70:73], v[170:173], v[202:205], v[70:73]
	v_mfma_f32_16x16x32_bf16 v[122:125], v[166:169], v[182:185], v[122:125]
	v_mfma_f32_16x16x32_bf16 v[118:121], v[174:177], v[182:185], v[118:121]
	v_mfma_f32_16x16x32_bf16 v[106:109], v[166:169], v[190:193], v[106:109]
	v_mfma_f32_16x16x32_bf16 v[102:105], v[174:177], v[190:193], v[102:105]
	v_mfma_f32_16x16x32_bf16 v[90:93], v[166:169], v[198:201], v[90:93]
	v_mfma_f32_16x16x32_bf16 v[86:89], v[174:177], v[198:201], v[86:89]
	v_mfma_f32_16x16x32_bf16 v[74:77], v[166:169], v[206:209], v[74:77]
	v_mfma_f32_16x16x32_bf16 v[70:73], v[174:177], v[206:209], v[70:73]
	s_barrier
	s_add_i32 s48, s62, s27
	v_lshl_add_u64 v[210:211], v[210:211], 0, s[66:67]
	s_mov_b32 m0, s48
	ds_read_b128 v[178:181], v149 offset:49152
	ds_read_b128 v[182:185], v149 offset:50176
	ds_read_b128 v[186:189], v149 offset:51200
	ds_read_b128 v[190:193], v149 offset:52224
	ds_read_b128 v[194:197], v149 offset:53248
	ds_read_b128 v[198:201], v149 offset:54272
	ds_read_b128 v[202:205], v149 offset:55296
	ds_read_b128 v[206:209], v149 offset:56320
	global_load_lds_dwordx4 v[210:211], off
	s_add_i32 m0, s48, 0x2000
	s_add_u32 s46, s46, 0x40080
	v_lshl_add_u64 v[210:211], v[212:213], 0, s[66:67]
	s_addc_u32 s47, s47, 0
	s_add_i32 s48, s63, s27
	global_load_lds_dwordx4 v[210:211], off
	v_lshl_add_u64 v[210:211], s[46:47], 0, v[0:1]
	s_mov_b32 m0, s48
	s_nop 0
	global_load_lds_dwordx4 v[210:211], off
	v_lshl_add_u64 v[210:211], s[46:47], 0, v[138:139]
	s_add_i32 m0, s48, 0x2000
	s_nop 0
	global_load_lds_dwordx4 v[210:211], off
	v_lshl_add_u64 v[210:211], v[216:217], 0, s[66:67]
	s_mov_b32 m0, s56
	s_nop 0
	global_load_lds_dwordx4 v[210:211], off
	v_lshl_add_u64 v[210:211], v[218:219], 0, s[66:67]
	s_mov_b32 m0, s57
	s_nop 0
	global_load_lds_dwordx4 v[210:211], off
	s_waitcnt vmcnt(8)
	s_waitcnt lgkmcnt(0)
	s_barrier
	s_waitcnt lgkmcnt(0)
	v_mfma_f32_16x16x32_bf16 v[66:69], v[144:147], v[178:181], v[66:69]
	v_mfma_f32_16x16x32_bf16 v[62:65], v[154:157], v[178:181], v[62:65]
	v_mfma_f32_16x16x32_bf16 v[50:53], v[144:147], v[186:189], v[50:53]
	v_mfma_f32_16x16x32_bf16 v[46:49], v[154:157], v[186:189], v[46:49]
	v_mfma_f32_16x16x32_bf16 v[34:37], v[144:147], v[194:197], v[34:37]
	v_mfma_f32_16x16x32_bf16 v[30:33], v[154:157], v[194:197], v[30:33]
	v_mfma_f32_16x16x32_bf16 v[18:21], v[144:147], v[202:205], v[18:21]
	v_mfma_f32_16x16x32_bf16 v[14:17], v[154:157], v[202:205], v[14:17]
	v_mfma_f32_16x16x32_bf16 v[66:69], v[150:153], v[182:185], v[66:69]
	v_mfma_f32_16x16x32_bf16 v[62:65], v[158:161], v[182:185], v[62:65]
	v_mfma_f32_16x16x32_bf16 v[50:53], v[150:153], v[190:193], v[50:53]
	v_mfma_f32_16x16x32_bf16 v[46:49], v[158:161], v[190:193], v[46:49]
	v_mfma_f32_16x16x32_bf16 v[34:37], v[150:153], v[198:201], v[34:37]
	v_mfma_f32_16x16x32_bf16 v[30:33], v[158:161], v[198:201], v[30:33]
	v_mfma_f32_16x16x32_bf16 v[18:21], v[150:153], v[206:209], v[18:21]
	v_mfma_f32_16x16x32_bf16 v[14:17], v[158:161], v[206:209], v[14:17]
	v_mfma_f32_16x16x32_bf16 v[58:61], v[162:165], v[178:181], v[58:61]
	v_mfma_f32_16x16x32_bf16 v[54:57], v[170:173], v[178:181], v[54:57]
	v_mfma_f32_16x16x32_bf16 v[42:45], v[162:165], v[186:189], v[42:45]
	v_mfma_f32_16x16x32_bf16 v[38:41], v[170:173], v[186:189], v[38:41]
	v_mfma_f32_16x16x32_bf16 v[26:29], v[162:165], v[194:197], v[26:29]
	v_mfma_f32_16x16x32_bf16 v[22:25], v[170:173], v[194:197], v[22:25]
	v_mfma_f32_16x16x32_bf16 v[10:13], v[162:165], v[202:205], v[10:13]
	v_mfma_f32_16x16x32_bf16 v[6:9], v[170:173], v[202:205], v[6:9]
	v_mfma_f32_16x16x32_bf16 v[58:61], v[166:169], v[182:185], v[58:61]
	v_mfma_f32_16x16x32_bf16 v[54:57], v[174:177], v[182:185], v[54:57]
	v_mfma_f32_16x16x32_bf16 v[42:45], v[166:169], v[190:193], v[42:45]
	v_mfma_f32_16x16x32_bf16 v[38:41], v[174:177], v[190:193], v[38:41]
	v_mfma_f32_16x16x32_bf16 v[26:29], v[166:169], v[198:201], v[26:29]
	v_mfma_f32_16x16x32_bf16 v[22:25], v[174:177], v[198:201], v[22:25]
	v_mfma_f32_16x16x32_bf16 v[10:13], v[166:169], v[206:209], v[10:13]
	v_mfma_f32_16x16x32_bf16 v[6:9], v[174:177], v[206:209], v[6:9]
	s_barrier
	s_add_i32 s61, s61, 2
	s_add_u32 s44, s44, 0x100
	s_addc_u32 s45, s45, 0
	s_add_u32 s59, s59, 0x100
	s_addc_u32 s60, s60, 0
	s_cmp_gt_u32 s61, 13
	s_cbranch_scc0 .LBB0_290
	s_and_b64 vcc, exec, s[30:31]
	s_cbranch_vccz .LBB0_293
	s_barrier

.Lrw_done_ip8_0:
	s_waitcnt lgkmcnt(0)
	s_barrier
	s_waitcnt lgkmcnt(0)
	v_mfma_scale_f32_16x16x128_f8f6f4 v[158:161], v[18:25], v[172:179], 0, v234, v235 op_sel_hi:[0,0,0]
	v_mfma_scale_f32_16x16x128_f8f6f4 v[154:157], v[26:33], v[172:179], 0, v234, v235 op_sel_hi:[0,0,0]
	v_mfma_scale_f32_16x16x128_f8f6f4 v[150:153], v[18:25], v[198:205], 0, v234, v235 op_sel_hi:[0,0,0]
	v_mfma_scale_f32_16x16x128_f8f6f4 v[146:149], v[26:33], v[198:205], 0, v234, v235 op_sel_hi:[0,0,0]
	v_mfma_scale_f32_16x16x128_f8f6f4 v[142:145], v[18:25], v[206:213], 0, v234, v235 op_sel_hi:[0,0,0]
	v_mfma_scale_f32_16x16x128_f8f6f4 v[138:141], v[26:33], v[206:213], 0, v234, v235 op_sel_hi:[0,0,0]
	v_mfma_scale_f32_16x16x128_f8f6f4 v[134:137], v[18:25], v[216:223], 0, v234, v235 op_sel_hi:[0,0,0]
	v_mfma_scale_f32_16x16x128_f8f6f4 v[130:133], v[26:33], v[216:223], 0, v234, v235 op_sel_hi:[0,0,0]
	v_mfma_scale_f32_16x16x128_f8f6f4 v[126:129], v[2:9], v[172:179], 0, v234, v235 op_sel_hi:[0,0,0]
	v_mfma_scale_f32_16x16x128_f8f6f4 v[122:125], v[10:17], v[172:179], 0, v234, v235 op_sel_hi:[0,0,0]
	v_mfma_scale_f32_16x16x128_f8f6f4 v[118:121], v[2:9], v[198:205], 0, v234, v235 op_sel_hi:[0,0,0]
	v_mfma_scale_f32_16x16x128_f8f6f4 v[114:117], v[10:17], v[198:205], 0, v234, v235 op_sel_hi:[0,0,0]
	v_mfma_scale_f32_16x16x128_f8f6f4 v[110:113], v[2:9], v[206:213], 0, v234, v235 op_sel_hi:[0,0,0]
	v_mfma_scale_f32_16x16x128_f8f6f4 v[106:109], v[10:17], v[206:213], 0, v234, v235 op_sel_hi:[0,0,0]
	v_mfma_scale_f32_16x16x128_f8f6f4 v[102:105], v[2:9], v[216:223], 0, v234, v235 op_sel_hi:[0,0,0]
	v_mfma_scale_f32_16x16x128_f8f6f4 v[98:101], v[10:17], v[216:223], 0, v234, v235 op_sel_hi:[0,0,0]
	s_barrier
	v_lshl_add_u64 v[172:173], s[44:45], 0, v[0:1]
	s_mov_b64 s[74:75], 0x100
	s_mov_b32 m0, s58
	v_lshl_add_u64 v[174:175], v[172:173], 0, s[74:75]
	ds_read_b128 v[198:201], v196 offset:16384
	ds_read_b128 v[202:205], v196 offset:17408
	ds_read_b128 v[206:209], v196 offset:18432
	ds_read_b128 v[210:213], v196 offset:19456
	ds_read_b128 v[216:219], v196 offset:20480
	ds_read_b128 v[220:223], v196 offset:21504
	ds_read_b128 v[224:227], v196 offset:22528
	ds_read_b128 v[228:231], v196 offset:23552
	global_load_lds_dwordx4 v[174:175], off
	v_lshl_add_u64 v[174:175], s[44:45], 0, v[166:167]
	s_add_u32 s48, s44, 0x20100
	v_lshl_add_u64 v[176:177], v[174:175], 0, s[74:75]
	s_mov_b32 m0, s59
	s_addc_u32 s49, s45, 0
	global_load_lds_dwordx4 v[176:177], off
	v_lshl_add_u64 v[176:177], s[48:49], 0, v[0:1]
	s_mov_b32 m0, s60
	s_nop 0
	global_load_lds_dwordx4 v[176:177], off
	v_lshl_add_u64 v[176:177], s[48:49], 0, v[166:167]
	s_mov_b32 m0, s61
	s_nop 0
	global_load_lds_dwordx4 v[176:177], off
	v_lshl_add_u64 v[176:177], s[46:47], 0, v[162:163]
	v_lshl_add_u64 v[178:179], v[176:177], 0, s[74:75]
	s_mov_b32 m0, s57
	s_nop 0
	global_load_lds_dwordx4 v[178:179], off
	v_lshl_add_u64 v[178:179], s[46:47], 0, v[164:165]
	v_lshl_add_u64 v[232:233], v[178:179], 0, s[74:75]
	s_mov_b32 m0, s62
	s_nop 0
	global_load_lds_dwordx4 v[232:233], off
	s_cmp_eq_u32 s50, 1
	s_cbranch_scc1 .Lrw_first_ip8_1
	s_waitcnt vmcnt(24)
	s_branch .Lrw_done_ip8_1

.Lrw_done_ip8_1:
	s_waitcnt lgkmcnt(0)
	s_barrier
	s_waitcnt lgkmcnt(0)
	v_mfma_scale_f32_16x16x128_f8f6f4 v[94:97], v[18:25], v[198:205], 0, v234, v235 op_sel_hi:[0,0,0]
	v_mfma_scale_f32_16x16x128_f8f6f4 v[90:93], v[26:33], v[198:205], 0, v234, v235 op_sel_hi:[0,0,0]
	v_mfma_scale_f32_16x16x128_f8f6f4 v[86:89], v[18:25], v[206:213], 0, v234, v235 op_sel_hi:[0,0,0]
	v_mfma_scale_f32_16x16x128_f8f6f4 v[82:85], v[26:33], v[206:213], 0, v234, v235 op_sel_hi:[0,0,0]
	v_mfma_scale_f32_16x16x128_f8f6f4 v[78:81], v[18:25], v[216:223], 0, v234, v235 op_sel_hi:[0,0,0]
	v_mfma_scale_f32_16x16x128_f8f6f4 v[74:77], v[26:33], v[216:223], 0, v234, v235 op_sel_hi:[0,0,0]
	v_mfma_scale_f32_16x16x128_f8f6f4 v[70:73], v[18:25], v[224:231], 0, v234, v235 op_sel_hi:[0,0,0]
	v_mfma_scale_f32_16x16x128_f8f6f4 v[66:69], v[26:33], v[224:231], 0, v234, v235 op_sel_hi:[0,0,0]
	v_mfma_scale_f32_16x16x128_f8f6f4 v[62:65], v[2:9], v[198:205], 0, v234, v235 op_sel_hi:[0,0,0]
	v_mfma_scale_f32_16x16x128_f8f6f4 v[58:61], v[10:17], v[198:205], 0, v234, v235 op_sel_hi:[0,0,0]
	v_mfma_scale_f32_16x16x128_f8f6f4 v[54:57], v[2:9], v[206:213], 0, v234, v235 op_sel_hi:[0,0,0]
	v_mfma_scale_f32_16x16x128_f8f6f4 v[50:53], v[10:17], v[206:213], 0, v234, v235 op_sel_hi:[0,0,0]
	v_mfma_scale_f32_16x16x128_f8f6f4 v[46:49], v[2:9], v[216:223], 0, v234, v235 op_sel_hi:[0,0,0]
	v_mfma_scale_f32_16x16x128_f8f6f4 v[42:45], v[10:17], v[216:223], 0, v234, v235 op_sel_hi:[0,0,0]
	v_mfma_scale_f32_16x16x128_f8f6f4 v[38:41], v[2:9], v[224:231], 0, v234, v235 op_sel_hi:[0,0,0]
	v_mfma_scale_f32_16x16x128_f8f6f4 v[34:37], v[10:17], v[224:231], 0, v234, v235 op_sel_hi:[0,0,0]
	s_barrier
	ds_read_b128 v[18:21], v188
	ds_read_b128 v[22:25], v189
	ds_read_b128 v[26:29], v190
	ds_read_b128 v[30:33], v191
	ds_read_b128 v[2:5], v192
	ds_read_b128 v[6:9], v193
	ds_read_b128 v[10:13], v194
	ds_read_b128 v[14:17], v195
	s_add_u32 s48, s46, 0x20100
	s_addc_u32 s49, s47, 0
	s_mov_b32 m0, s63
	v_lshl_add_u64 v[232:233], s[48:49], 0, v[162:163]
	ds_read_b128 v[198:201], v196 offset:32768
	ds_read_b128 v[202:205], v196 offset:33792
	ds_read_b128 v[206:209], v196 offset:34816
	ds_read_b128 v[210:213], v196 offset:35840
	ds_read_b128 v[216:219], v196 offset:36864
	ds_read_b128 v[220:223], v196 offset:37888
	ds_read_b128 v[224:227], v196 offset:38912
	ds_read_b128 v[228:231], v196 offset:39936
	global_load_lds_dwordx4 v[232:233], off
	v_lshl_add_u64 v[232:233], s[48:49], 0, v[164:165]
	s_mov_b32 m0, s64
	s_nop 0
	global_load_lds_dwordx4 v[232:233], off
	s_waitcnt vmcnt(8)
	s_waitcnt lgkmcnt(0)
	s_barrier
	s_waitcnt lgkmcnt(0)
	v_mfma_scale_f32_16x16x128_f8f6f4 v[158:161], v[18:25], v[198:205], v[158:161], v234, v235 op_sel_hi:[0,0,0]
	v_mfma_scale_f32_16x16x128_f8f6f4 v[154:157], v[26:33], v[198:205], v[154:157], v234, v235 op_sel_hi:[0,0,0]
	v_mfma_scale_f32_16x16x128_f8f6f4 v[150:153], v[18:25], v[206:213], v[150:153], v234, v235 op_sel_hi:[0,0,0]
	v_mfma_scale_f32_16x16x128_f8f6f4 v[146:149], v[26:33], v[206:213], v[146:149], v234, v235 op_sel_hi:[0,0,0]
	v_mfma_scale_f32_16x16x128_f8f6f4 v[142:145], v[18:25], v[216:223], v[142:145], v234, v235 op_sel_hi:[0,0,0]
	v_mfma_scale_f32_16x16x128_f8f6f4 v[138:141], v[26:33], v[216:223], v[138:141], v234, v235 op_sel_hi:[0,0,0]
	v_mfma_scale_f32_16x16x128_f8f6f4 v[134:137], v[18:25], v[224:231], v[134:137], v234, v235 op_sel_hi:[0,0,0]
	v_mfma_scale_f32_16x16x128_f8f6f4 v[130:133], v[26:33], v[224:231], v[130:133], v234, v235 op_sel_hi:[0,0,0]
	v_mfma_scale_f32_16x16x128_f8f6f4 v[126:129], v[2:9], v[198:205], v[126:129], v234, v235 op_sel_hi:[0,0,0]
	v_mfma_scale_f32_16x16x128_f8f6f4 v[122:125], v[10:17], v[198:205], v[122:125], v234, v235 op_sel_hi:[0,0,0]
	v_mfma_scale_f32_16x16x128_f8f6f4 v[118:121], v[2:9], v[206:213], v[118:121], v234, v235 op_sel_hi:[0,0,0]
	v_mfma_scale_f32_16x16x128_f8f6f4 v[114:117], v[10:17], v[206:213], v[114:117], v234, v235 op_sel_hi:[0,0,0]
	v_mfma_scale_f32_16x16x128_f8f6f4 v[110:113], v[2:9], v[216:223], v[110:113], v234, v235 op_sel_hi:[0,0,0]
	v_mfma_scale_f32_16x16x128_f8f6f4 v[106:109], v[10:17], v[216:223], v[106:109], v234, v235 op_sel_hi:[0,0,0]
	v_mfma_scale_f32_16x16x128_f8f6f4 v[102:105], v[2:9], v[224:231], v[102:105], v234, v235 op_sel_hi:[0,0,0]
	v_mfma_scale_f32_16x16x128_f8f6f4 v[98:101], v[10:17], v[224:231], v[98:101], v234, v235 op_sel_hi:[0,0,0]
	s_barrier
	s_mov_b64 s[74:75], 0x180
	s_mov_b32 m0, s7
	v_lshl_add_u64 v[172:173], v[172:173], 0, s[74:75]
	s_add_u32 s48, s44, 0x20180
	ds_read_b128 v[198:201], v196 offset:49152
	ds_read_b128 v[202:205], v196 offset:50176
	ds_read_b128 v[206:209], v196 offset:51200
	ds_read_b128 v[210:213], v196 offset:52224
	ds_read_b128 v[216:219], v196 offset:53248
	ds_read_b128 v[220:223], v196 offset:54272
	ds_read_b128 v[224:227], v196 offset:55296
	ds_read_b128 v[228:231], v196 offset:56320
	global_load_lds_dwordx4 v[172:173], off
	v_lshl_add_u64 v[172:173], v[174:175], 0, s[74:75]
	s_mov_b32 m0, s65
	s_addc_u32 s49, s45, 0
	global_load_lds_dwordx4 v[172:173], off
	v_lshl_add_u64 v[172:173], s[48:49], 0, v[0:1]
	s_mov_b32 m0, s13
	s_nop 0
	global_load_lds_dwordx4 v[172:173], off
	v_lshl_add_u64 v[172:173], s[48:49], 0, v[166:167]
	s_mov_b32 m0, s51
	s_nop 0
	global_load_lds_dwordx4 v[172:173], off
	v_lshl_add_u64 v[172:173], v[176:177], 0, s[74:75]
	s_mov_b32 m0, s68
	s_nop 0
	global_load_lds_dwordx4 v[172:173], off
	v_lshl_add_u64 v[172:173], v[178:179], 0, s[74:75]
	s_mov_b32 m0, s52
	s_nop 0
	global_load_lds_dwordx4 v[172:173], off
	s_waitcnt vmcnt(8)
	s_waitcnt lgkmcnt(0)
	s_barrier
	s_waitcnt lgkmcnt(0)
	v_mfma_scale_f32_16x16x128_f8f6f4 v[94:97], v[18:25], v[198:205], v[94:97], v234, v235 op_sel_hi:[0,0,0]
	v_mfma_scale_f32_16x16x128_f8f6f4 v[90:93], v[26:33], v[198:205], v[90:93], v234, v235 op_sel_hi:[0,0,0]
	v_mfma_scale_f32_16x16x128_f8f6f4 v[86:89], v[18:25], v[206:213], v[86:89], v234, v235 op_sel_hi:[0,0,0]
	v_mfma_scale_f32_16x16x128_f8f6f4 v[82:85], v[26:33], v[206:213], v[82:85], v234, v235 op_sel_hi:[0,0,0]
	v_mfma_scale_f32_16x16x128_f8f6f4 v[78:81], v[18:25], v[216:223], v[78:81], v234, v235 op_sel_hi:[0,0,0]
	v_mfma_scale_f32_16x16x128_f8f6f4 v[74:77], v[26:33], v[216:223], v[74:77], v234, v235 op_sel_hi:[0,0,0]
	v_mfma_scale_f32_16x16x128_f8f6f4 v[70:73], v[18:25], v[224:231], v[70:73], v234, v235 op_sel_hi:[0,0,0]
	v_mfma_scale_f32_16x16x128_f8f6f4 v[66:69], v[26:33], v[224:231], v[66:69], v234, v235 op_sel_hi:[0,0,0]
	v_mfma_scale_f32_16x16x128_f8f6f4 v[62:65], v[2:9], v[198:205], v[62:65], v234, v235 op_sel_hi:[0,0,0]
	v_mfma_scale_f32_16x16x128_f8f6f4 v[58:61], v[10:17], v[198:205], v[58:61], v234, v235 op_sel_hi:[0,0,0]
	v_mfma_scale_f32_16x16x128_f8f6f4 v[54:57], v[2:9], v[206:213], v[54:57], v234, v235 op_sel_hi:[0,0,0]
	v_mfma_scale_f32_16x16x128_f8f6f4 v[50:53], v[10:17], v[206:213], v[50:53], v234, v235 op_sel_hi:[0,0,0]
	v_mfma_scale_f32_16x16x128_f8f6f4 v[46:49], v[2:9], v[216:223], v[46:49], v234, v235 op_sel_hi:[0,0,0]
	v_mfma_scale_f32_16x16x128_f8f6f4 v[42:45], v[10:17], v[216:223], v[42:45], v234, v235 op_sel_hi:[0,0,0]
	v_mfma_scale_f32_16x16x128_f8f6f4 v[38:41], v[2:9], v[224:231], v[38:41], v234, v235 op_sel_hi:[0,0,0]
	v_mfma_scale_f32_16x16x128_f8f6f4 v[34:37], v[10:17], v[224:231], v[34:37], v234, v235 op_sel_hi:[0,0,0]
	s_barrier
	s_add_u32 s46, s46, 0x20180
	s_addc_u32 s47, s47, 0
	s_add_u32 s37, s44, 0x200
	s_addc_u32 s74, s45, 0
	s_mov_b32 s75, 0
.LBB0_388:
	ds_read_b128 v[2:5], v180
	ds_read_b128 v[6:9], v181
	ds_read_b128 v[10:13], v182
	ds_read_b128 v[14:17], v183
	ds_read_b128 v[26:29], v184
	ds_read_b128 v[30:33], v185
	ds_read_b128 v[172:175], v186
	ds_read_b128 v[176:179], v187
	s_add_u32 s44, s46, 0xfffe0080
	s_addc_u32 s45, s47, -1
	s_cmp_eq_u32 s75, 4
	s_cselect_b32 s49, s1, s45
	s_cselect_b32 s48, s5, s44
	s_cselect_b32 s45, s23, s74
	s_cselect_b32 s44, s26, s37
	s_mov_b32 m0, s27
	v_lshl_add_u64 v[224:225], s[46:47], 0, v[168:169]
	ds_read_b128 v[18:21], v196
	ds_read_b128 v[22:25], v196 offset:1024
	ds_read_b128 v[198:201], v196 offset:2048
	ds_read_b128 v[202:205], v196 offset:3072
	ds_read_b128 v[206:209], v196 offset:4096
	ds_read_b128 v[210:213], v196 offset:5120
	ds_read_b128 v[216:219], v196 offset:6144
	ds_read_b128 v[220:223], v196 offset:7168
	global_load_lds_dwordx4 v[224:225], off
	v_lshl_add_u64 v[224:225], s[46:47], 0, v[170:171]
	s_mov_b32 m0, s35
	s_nop 0
	global_load_lds_dwordx4 v[224:225], off
	s_waitcnt vmcnt(8)
	s_waitcnt lgkmcnt(0)
	s_barrier
	s_waitcnt lgkmcnt(0)
	v_mfma_scale_f32_16x16x128_f8f6f4 v[158:161], v[2:9], v[18:25], v[158:161], v234, v235 op_sel_hi:[0,0,0]
	v_mfma_scale_f32_16x16x128_f8f6f4 v[154:157], v[10:17], v[18:25], v[154:157], v234, v235 op_sel_hi:[0,0,0]
	v_mfma_scale_f32_16x16x128_f8f6f4 v[150:153], v[2:9], v[198:205], v[150:153], v234, v235 op_sel_hi:[0,0,0]
	v_mfma_scale_f32_16x16x128_f8f6f4 v[146:149], v[10:17], v[198:205], v[146:149], v234, v235 op_sel_hi:[0,0,0]
	v_mfma_scale_f32_16x16x128_f8f6f4 v[142:145], v[2:9], v[206:213], v[142:145], v234, v235 op_sel_hi:[0,0,0]
	v_mfma_scale_f32_16x16x128_f8f6f4 v[138:141], v[10:17], v[206:213], v[138:141], v234, v235 op_sel_hi:[0,0,0]
	v_mfma_scale_f32_16x16x128_f8f6f4 v[134:137], v[2:9], v[216:223], v[134:137], v234, v235 op_sel_hi:[0,0,0]
	v_mfma_scale_f32_16x16x128_f8f6f4 v[130:133], v[10:17], v[216:223], v[130:133], v234, v235 op_sel_hi:[0,0,0]
	v_mfma_scale_f32_16x16x128_f8f6f4 v[126:129], v[26:33], v[18:25], v[126:129], v234, v235 op_sel_hi:[0,0,0]
	v_mfma_scale_f32_16x16x128_f8f6f4 v[122:125], v[172:179], v[18:25], v[122:125], v234, v235 op_sel_hi:[0,0,0]
	v_mfma_scale_f32_16x16x128_f8f6f4 v[118:121], v[26:33], v[198:205], v[118:121], v234, v235 op_sel_hi:[0,0,0]
	v_mfma_scale_f32_16x16x128_f8f6f4 v[114:117], v[172:179], v[198:205], v[114:117], v234, v235 op_sel_hi:[0,0,0]
	v_mfma_scale_f32_16x16x128_f8f6f4 v[110:113], v[26:33], v[206:213], v[110:113], v234, v235 op_sel_hi:[0,0,0]
	v_mfma_scale_f32_16x16x128_f8f6f4 v[106:109], v[172:179], v[206:213], v[106:109], v234, v235 op_sel_hi:[0,0,0]
	v_mfma_scale_f32_16x16x128_f8f6f4 v[102:105], v[26:33], v[216:223], v[102:105], v234, v235 op_sel_hi:[0,0,0]
	v_mfma_scale_f32_16x16x128_f8f6f4 v[98:101], v[172:179], v[216:223], v[98:101], v234, v235 op_sel_hi:[0,0,0]
	s_barrier
	s_mov_b32 m0, s58
	v_lshl_add_u64 v[18:19], s[44:45], 0, v[0:1]
	s_add_u32 vcc_lo, s44, 0x20000
	ds_read_b128 v[198:201], v196 offset:16384
	ds_read_b128 v[202:205], v196 offset:17408
	ds_read_b128 v[206:209], v196 offset:18432
	ds_read_b128 v[210:213], v196 offset:19456
	ds_read_b128 v[216:219], v196 offset:20480
	ds_read_b128 v[220:223], v196 offset:21504
	ds_read_b128 v[224:227], v196 offset:22528
	ds_read_b128 v[228:231], v196 offset:23552
	global_load_lds_dwordx4 v[18:19], off
	v_lshl_add_u64 v[20:21], s[44:45], 0, v[166:167]
	s_mov_b32 m0, s59
	s_addc_u32 vcc_hi, s45, 0
	global_load_lds_dwordx4 v[20:21], off
	v_lshl_add_u64 v[22:23], vcc, 0, v[0:1]
	s_mov_b32 m0, s60
	v_lshl_add_u64 v[24:25], s[48:49], 0, v[164:165]
	global_load_lds_dwordx4 v[22:23], off
	v_lshl_add_u64 v[22:23], vcc, 0, v[166:167]
	s_mov_b32 m0, s61
	s_nop 0
	global_load_lds_dwordx4 v[22:23], off
	v_lshl_add_u64 v[22:23], s[48:49], 0, v[162:163]
	s_mov_b32 m0, s57
	s_nop 0
	global_load_lds_dwordx4 v[22:23], off
	s_mov_b32 m0, s62
	s_nop 0
	global_load_lds_dwordx4 v[24:25], off
	s_waitcnt vmcnt(8)
	s_waitcnt lgkmcnt(0)
	s_barrier
	s_waitcnt lgkmcnt(0)
	v_mfma_scale_f32_16x16x128_f8f6f4 v[94:97], v[2:9], v[198:205], v[94:97], v234, v235 op_sel_hi:[0,0,0]
	v_mfma_scale_f32_16x16x128_f8f6f4 v[90:93], v[10:17], v[198:205], v[90:93], v234, v235 op_sel_hi:[0,0,0]
	v_mfma_scale_f32_16x16x128_f8f6f4 v[86:89], v[2:9], v[206:213], v[86:89], v234, v235 op_sel_hi:[0,0,0]
	v_mfma_scale_f32_16x16x128_f8f6f4 v[82:85], v[10:17], v[206:213], v[82:85], v234, v235 op_sel_hi:[0,0,0]
	v_mfma_scale_f32_16x16x128_f8f6f4 v[78:81], v[2:9], v[216:223], v[78:81], v234, v235 op_sel_hi:[0,0,0]
	v_mfma_scale_f32_16x16x128_f8f6f4 v[74:77], v[10:17], v[216:223], v[74:77], v234, v235 op_sel_hi:[0,0,0]
	v_mfma_scale_f32_16x16x128_f8f6f4 v[70:73], v[2:9], v[224:231], v[70:73], v234, v235 op_sel_hi:[0,0,0]
	v_mfma_scale_f32_16x16x128_f8f6f4 v[66:69], v[10:17], v[224:231], v[66:69], v234, v235 op_sel_hi:[0,0,0]
	v_mfma_scale_f32_16x16x128_f8f6f4 v[62:65], v[26:33], v[198:205], v[62:65], v234, v235 op_sel_hi:[0,0,0]
	v_mfma_scale_f32_16x16x128_f8f6f4 v[58:61], v[172:179], v[198:205], v[58:61], v234, v235 op_sel_hi:[0,0,0]
	v_mfma_scale_f32_16x16x128_f8f6f4 v[54:57], v[26:33], v[206:213], v[54:57], v234, v235 op_sel_hi:[0,0,0]
	v_mfma_scale_f32_16x16x128_f8f6f4 v[50:53], v[172:179], v[206:213], v[50:53], v234, v235 op_sel_hi:[0,0,0]
	v_mfma_scale_f32_16x16x128_f8f6f4 v[46:49], v[26:33], v[216:223], v[46:49], v234, v235 op_sel_hi:[0,0,0]
	v_mfma_scale_f32_16x16x128_f8f6f4 v[42:45], v[172:179], v[216:223], v[42:45], v234, v235 op_sel_hi:[0,0,0]
	v_mfma_scale_f32_16x16x128_f8f6f4 v[38:41], v[26:33], v[224:231], v[38:41], v234, v235 op_sel_hi:[0,0,0]
	v_mfma_scale_f32_16x16x128_f8f6f4 v[34:37], v[172:179], v[224:231], v[34:37], v234, v235 op_sel_hi:[0,0,0]
	s_barrier
	ds_read_b128 v[10:13], v188
	ds_read_b128 v[14:17], v189
	ds_read_b128 v[26:29], v190
	ds_read_b128 v[30:33], v191
	ds_read_b128 v[2:5], v192
	ds_read_b128 v[6:9], v193
	ds_read_b128 v[172:175], v194
	ds_read_b128 v[176:179], v195
	s_add_u32 s48, s48, 0x20000
	s_addc_u32 s49, s49, 0
	s_mov_b32 m0, s63
	v_lshl_add_u64 v[232:233], s[48:49], 0, v[162:163]
	ds_read_b128 v[198:201], v196 offset:32768
	ds_read_b128 v[202:205], v196 offset:33792
	ds_read_b128 v[206:209], v196 offset:34816
	ds_read_b128 v[210:213], v196 offset:35840
	ds_read_b128 v[216:219], v196 offset:36864
	ds_read_b128 v[220:223], v196 offset:37888
	ds_read_b128 v[224:227], v196 offset:38912
	ds_read_b128 v[228:231], v196 offset:39936
	global_load_lds_dwordx4 v[232:233], off
	v_lshl_add_u64 v[232:233], s[48:49], 0, v[164:165]
	s_mov_b32 m0, s64
	s_nop 0
	global_load_lds_dwordx4 v[232:233], off
	s_waitcnt vmcnt(8)
	s_waitcnt lgkmcnt(0)
	s_barrier
	s_waitcnt lgkmcnt(0)
	v_mfma_scale_f32_16x16x128_f8f6f4 v[158:161], v[10:17], v[198:205], v[158:161], v234, v235 op_sel_hi:[0,0,0]
	v_mfma_scale_f32_16x16x128_f8f6f4 v[154:157], v[26:33], v[198:205], v[154:157], v234, v235 op_sel_hi:[0,0,0]
	v_mfma_scale_f32_16x16x128_f8f6f4 v[150:153], v[10:17], v[206:213], v[150:153], v234, v235 op_sel_hi:[0,0,0]
	v_mfma_scale_f32_16x16x128_f8f6f4 v[146:149], v[26:33], v[206:213], v[146:149], v234, v235 op_sel_hi:[0,0,0]
	v_mfma_scale_f32_16x16x128_f8f6f4 v[142:145], v[10:17], v[216:223], v[142:145], v234, v235 op_sel_hi:[0,0,0]
	v_mfma_scale_f32_16x16x128_f8f6f4 v[138:141], v[26:33], v[216:223], v[138:141], v234, v235 op_sel_hi:[0,0,0]
	v_mfma_scale_f32_16x16x128_f8f6f4 v[134:137], v[10:17], v[224:231], v[134:137], v234, v235 op_sel_hi:[0,0,0]
	v_mfma_scale_f32_16x16x128_f8f6f4 v[130:133], v[26:33], v[224:231], v[130:133], v234, v235 op_sel_hi:[0,0,0]
	v_mfma_scale_f32_16x16x128_f8f6f4 v[126:129], v[2:9], v[198:205], v[126:129], v234, v235 op_sel_hi:[0,0,0]
	v_mfma_scale_f32_16x16x128_f8f6f4 v[122:125], v[172:179], v[198:205], v[122:125], v234, v235 op_sel_hi:[0,0,0]
	v_mfma_scale_f32_16x16x128_f8f6f4 v[118:121], v[2:9], v[206:213], v[118:121], v234, v235 op_sel_hi:[0,0,0]
	v_mfma_scale_f32_16x16x128_f8f6f4 v[114:117], v[172:179], v[206:213], v[114:117], v234, v235 op_sel_hi:[0,0,0]
	v_mfma_scale_f32_16x16x128_f8f6f4 v[110:113], v[2:9], v[216:223], v[110:113], v234, v235 op_sel_hi:[0,0,0]
	v_mfma_scale_f32_16x16x128_f8f6f4 v[106:109], v[172:179], v[216:223], v[106:109], v234, v235 op_sel_hi:[0,0,0]
	v_mfma_scale_f32_16x16x128_f8f6f4 v[102:105], v[2:9], v[224:231], v[102:105], v234, v235 op_sel_hi:[0,0,0]
	v_mfma_scale_f32_16x16x128_f8f6f4 v[98:101], v[172:179], v[224:231], v[98:101], v234, v235 op_sel_hi:[0,0,0]
	s_barrier
	s_mov_b32 m0, s7
	v_lshl_add_u64 v[18:19], v[18:19], 0, s[66:67]
	s_add_u32 s44, s44, 0x20080
	ds_read_b128 v[198:201], v196 offset:49152
	ds_read_b128 v[202:205], v196 offset:50176
	ds_read_b128 v[206:209], v196 offset:51200
	ds_read_b128 v[210:213], v196 offset:52224
	ds_read_b128 v[216:219], v196 offset:53248
	ds_read_b128 v[220:223], v196 offset:54272
	ds_read_b128 v[224:227], v196 offset:55296
	ds_read_b128 v[228:231], v196 offset:56320
	global_load_lds_dwordx4 v[18:19], off
	v_lshl_add_u64 v[18:19], v[20:21], 0, s[66:67]
	s_mov_b32 m0, s65
	s_addc_u32 s45, s45, 0
	global_load_lds_dwordx4 v[18:19], off
	v_lshl_add_u64 v[18:19], s[44:45], 0, v[0:1]
	s_mov_b32 m0, s13
	s_nop 0
	global_load_lds_dwordx4 v[18:19], off
	v_lshl_add_u64 v[18:19], s[44:45], 0, v[166:167]
	s_mov_b32 m0, s51
	s_nop 0
	global_load_lds_dwordx4 v[18:19], off
	v_lshl_add_u64 v[18:19], v[22:23], 0, s[66:67]
	s_mov_b32 m0, s68
	s_nop 0
	global_load_lds_dwordx4 v[18:19], off
	v_lshl_add_u64 v[18:19], v[24:25], 0, s[66:67]
	s_mov_b32 m0, s52
	s_nop 0
	global_load_lds_dwordx4 v[18:19], off
	s_waitcnt vmcnt(8)
	s_waitcnt lgkmcnt(0)
	s_barrier
	s_waitcnt lgkmcnt(0)
	v_mfma_scale_f32_16x16x128_f8f6f4 v[94:97], v[10:17], v[198:205], v[94:97], v234, v235 op_sel_hi:[0,0,0]
	v_mfma_scale_f32_16x16x128_f8f6f4 v[90:93], v[26:33], v[198:205], v[90:93], v234, v235 op_sel_hi:[0,0,0]
	v_mfma_scale_f32_16x16x128_f8f6f4 v[86:89], v[10:17], v[206:213], v[86:89], v234, v235 op_sel_hi:[0,0,0]
	v_mfma_scale_f32_16x16x128_f8f6f4 v[82:85], v[26:33], v[206:213], v[82:85], v234, v235 op_sel_hi:[0,0,0]
	v_mfma_scale_f32_16x16x128_f8f6f4 v[78:81], v[10:17], v[216:223], v[78:81], v234, v235 op_sel_hi:[0,0,0]
	v_mfma_scale_f32_16x16x128_f8f6f4 v[74:77], v[26:33], v[216:223], v[74:77], v234, v235 op_sel_hi:[0,0,0]
	v_mfma_scale_f32_16x16x128_f8f6f4 v[70:73], v[10:17], v[224:231], v[70:73], v234, v235 op_sel_hi:[0,0,0]
	v_mfma_scale_f32_16x16x128_f8f6f4 v[66:69], v[26:33], v[224:231], v[66:69], v234, v235 op_sel_hi:[0,0,0]
	v_mfma_scale_f32_16x16x128_f8f6f4 v[62:65], v[2:9], v[198:205], v[62:65], v234, v235 op_sel_hi:[0,0,0]
	v_mfma_scale_f32_16x16x128_f8f6f4 v[58:61], v[172:179], v[198:205], v[58:61], v234, v235 op_sel_hi:[0,0,0]
	v_mfma_scale_f32_16x16x128_f8f6f4 v[54:57], v[2:9], v[206:213], v[54:57], v234, v235 op_sel_hi:[0,0,0]
	v_mfma_scale_f32_16x16x128_f8f6f4 v[50:53], v[172:179], v[206:213], v[50:53], v234, v235 op_sel_hi:[0,0,0]
	v_mfma_scale_f32_16x16x128_f8f6f4 v[46:49], v[2:9], v[216:223], v[46:49], v234, v235 op_sel_hi:[0,0,0]
	v_mfma_scale_f32_16x16x128_f8f6f4 v[42:45], v[172:179], v[216:223], v[42:45], v234, v235 op_sel_hi:[0,0,0]
	v_mfma_scale_f32_16x16x128_f8f6f4 v[38:41], v[2:9], v[224:231], v[38:41], v234, v235 op_sel_hi:[0,0,0]
	v_mfma_scale_f32_16x16x128_f8f6f4 v[34:37], v[172:179], v[224:231], v[34:37], v234, v235 op_sel_hi:[0,0,0]
	s_barrier
	s_add_i32 s75, s75, 2
	s_add_u32 s46, s46, 0x100
	s_addc_u32 s47, s47, 0
	s_add_u32 s37, s37, 0x100
	s_addc_u32 s74, s74, 0
	s_cmp_gt_u32 s75, 5
	s_cbranch_scc0 .LBB0_388
	s_and_b64 vcc, exec, s[30:31]
	s_cbranch_vccz .LBB0_391
	s_barrier

.LBB0_1368:
	v_add_u32_e32 v134, 0x10000, v226
	v_add_u32_e32 v146, 0x14000, v226
	ds_read_b128 v[150:153], v134
	ds_read_b128 v[154:157], v134 offset:1024
	ds_read_b128 v[158:161], v134 offset:2048
	ds_read_b128 v[162:165], v134 offset:3072
	s_waitcnt vmcnt(0)
	ds_read_b128 v[134:137], v146
	ds_read_b128 v[138:141], v146 offset:1024
	ds_read_b128 v[142:145], v146 offset:2048
	ds_read_b128 v[146:149], v146 offset:3072
	v_lshl_add_u64 v[208:209], s[44:45], 0, v[204:205]
	s_add_i32 m0, s52, 0xc000
	s_waitcnt lgkmcnt(0)
	ds_read_b128 v[178:181], v227
	ds_read_b128 v[194:197], v227 offset:1024
	ds_read_b128 v[174:177], v227 offset:2048
	ds_read_b128 v[190:193], v227 offset:3072
	ds_read_b128 v[170:173], v227 offset:4096
	ds_read_b128 v[186:189], v227 offset:5120
	ds_read_b128 v[166:169], v227 offset:6144
	ds_read_b128 v[182:185], v227 offset:7168
	global_load_lds_dwordx4 v[208:209], off
	v_lshl_add_u64 v[208:209], s[44:45], 0, v[206:207]
	s_add_i32 m0, s52, 0xe000
	s_nop 0
	global_load_lds_dwordx4 v[208:209], off
	s_waitcnt vmcnt(8)
	s_waitcnt lgkmcnt(0)
	s_barrier
	s_waitcnt lgkmcnt(0)
	v_mfma_f32_16x16x32_bf16 v[130:133], v[150:153], v[178:181], v[130:133]
	v_mfma_f32_16x16x32_bf16 v[126:129], v[158:161], v[178:181], v[126:129]
	v_mfma_f32_16x16x32_bf16 v[122:125], v[150:153], v[174:177], v[122:125]
	v_mfma_f32_16x16x32_bf16 v[118:121], v[158:161], v[174:177], v[118:121]
	v_mfma_f32_16x16x32_bf16 v[114:117], v[150:153], v[170:173], v[114:117]
	v_mfma_f32_16x16x32_bf16 v[110:113], v[158:161], v[170:173], v[110:113]
	v_mfma_f32_16x16x32_bf16 v[106:109], v[150:153], v[166:169], v[106:109]
	v_mfma_f32_16x16x32_bf16 v[102:105], v[158:161], v[166:169], v[102:105]
	v_mfma_f32_16x16x32_bf16 v[130:133], v[154:157], v[194:197], v[130:133]
	v_mfma_f32_16x16x32_bf16 v[126:129], v[162:165], v[194:197], v[126:129]
	v_mfma_f32_16x16x32_bf16 v[122:125], v[154:157], v[190:193], v[122:125]
	v_mfma_f32_16x16x32_bf16 v[118:121], v[162:165], v[190:193], v[118:121]
	v_mfma_f32_16x16x32_bf16 v[114:117], v[154:157], v[186:189], v[114:117]
	v_mfma_f32_16x16x32_bf16 v[110:113], v[162:165], v[186:189], v[110:113]
	v_mfma_f32_16x16x32_bf16 v[106:109], v[154:157], v[182:185], v[106:109]
	v_mfma_f32_16x16x32_bf16 v[102:105], v[162:165], v[182:185], v[102:105]
	v_mfma_f32_16x16x32_bf16 v[98:101], v[134:137], v[178:181], v[98:101]
	v_mfma_f32_16x16x32_bf16 v[94:97], v[142:145], v[178:181], v[94:97]
	v_mfma_f32_16x16x32_bf16 v[90:93], v[134:137], v[174:177], v[90:93]
	v_mfma_f32_16x16x32_bf16 v[86:89], v[142:145], v[174:177], v[86:89]
	v_mfma_f32_16x16x32_bf16 v[82:85], v[134:137], v[170:173], v[82:85]
	v_mfma_f32_16x16x32_bf16 v[78:81], v[142:145], v[170:173], v[78:81]
	v_mfma_f32_16x16x32_bf16 v[74:77], v[134:137], v[166:169], v[74:77]
	v_mfma_f32_16x16x32_bf16 v[70:73], v[142:145], v[166:169], v[70:73]
	v_mfma_f32_16x16x32_bf16 v[98:101], v[138:141], v[194:197], v[98:101]
	v_mfma_f32_16x16x32_bf16 v[94:97], v[146:149], v[194:197], v[94:97]
	v_mfma_f32_16x16x32_bf16 v[90:93], v[138:141], v[190:193], v[90:93]
	v_mfma_f32_16x16x32_bf16 v[86:89], v[146:149], v[190:193], v[86:89]
	v_mfma_f32_16x16x32_bf16 v[82:85], v[138:141], v[186:189], v[82:85]
	v_mfma_f32_16x16x32_bf16 v[78:81], v[146:149], v[186:189], v[78:81]
	v_mfma_f32_16x16x32_bf16 v[74:77], v[138:141], v[182:185], v[74:77]
	v_mfma_f32_16x16x32_bf16 v[70:73], v[146:149], v[182:185], v[70:73]
	s_barrier
	v_cndmask_b32_e64 v208, 0, 1, s[6:7]
	v_cmp_ne_u32_e64 s[8:9], 1, v208
	s_andn2_b64 vcc, exec, s[6:7]
	s_cbranch_vccnz .LBB0_1370
	ds_read_b128 v[178:181], v227 offset:16384
	ds_read_b128 v[194:197], v227 offset:17408
	ds_read_b128 v[174:177], v227 offset:18432
	ds_read_b128 v[190:193], v227 offset:19456
	ds_read_b128 v[170:173], v227 offset:20480
	ds_read_b128 v[186:189], v227 offset:21504
	ds_read_b128 v[166:169], v227 offset:22528
	ds_read_b128 v[182:185], v227 offset:23552
.LBB0_1370:
	s_add_u32 s46, s44, 0xfffa0080
	s_addc_u32 s47, s45, -1
	s_cmp_eq_u32 s83, 4
	s_cselect_b32 s49, s41, s47
	s_cselect_b32 s48, s40, s46
	s_cselect_b32 s47, s27, s75
	s_cselect_b32 s46, s39, s74
	s_mov_b32 m0, s53
	v_lshl_add_u64 v[208:209], s[46:47], 0, v[0:1]
	s_add_u32 vcc_lo, s46, 0x20000
	global_load_lds_dwordx4 v[208:209], off
	v_lshl_add_u64 v[210:211], s[46:47], 0, v[202:203]
	s_mov_b32 m0, s54
	s_addc_u32 vcc_hi, s47, 0
	global_load_lds_dwordx4 v[210:211], off
	v_lshl_add_u64 v[212:213], vcc, 0, v[0:1]
	s_mov_b32 m0, s55
	v_lshl_add_u64 v[216:217], s[48:49], 0, v[200:201]
	global_load_lds_dwordx4 v[212:213], off
	v_lshl_add_u64 v[212:213], vcc, 0, v[202:203]
	s_mov_b32 m0, s56
	s_and_b64 vcc, exec, s[8:9]
	global_load_lds_dwordx4 v[212:213], off
	v_lshl_add_u64 v[212:213], s[48:49], 0, v[198:199]
	s_mov_b32 m0, s52
	s_nop 0
	global_load_lds_dwordx4 v[212:213], off
	s_mov_b32 m0, s57
	s_nop 0
	global_load_lds_dwordx4 v[216:217], off
	s_waitcnt vmcnt(8)
	s_waitcnt lgkmcnt(0)
	s_barrier
	s_cbranch_vccnz .LBB0_1372
	s_waitcnt lgkmcnt(0)
	v_mfma_f32_16x16x32_bf16 v[66:69], v[150:153], v[178:181], v[66:69]
	v_mfma_f32_16x16x32_bf16 v[62:65], v[158:161], v[178:181], v[62:65]
	v_mfma_f32_16x16x32_bf16 v[58:61], v[150:153], v[174:177], v[58:61]
	v_mfma_f32_16x16x32_bf16 v[54:57], v[158:161], v[174:177], v[54:57]
	v_mfma_f32_16x16x32_bf16 v[50:53], v[150:153], v[170:173], v[50:53]
	v_mfma_f32_16x16x32_bf16 v[46:49], v[158:161], v[170:173], v[46:49]
	v_mfma_f32_16x16x32_bf16 v[42:45], v[150:153], v[166:169], v[42:45]
	v_mfma_f32_16x16x32_bf16 v[38:41], v[158:161], v[166:169], v[38:41]
	v_mfma_f32_16x16x32_bf16 v[66:69], v[154:157], v[194:197], v[66:69]
	v_mfma_f32_16x16x32_bf16 v[62:65], v[162:165], v[194:197], v[62:65]
	v_mfma_f32_16x16x32_bf16 v[58:61], v[154:157], v[190:193], v[58:61]
	v_mfma_f32_16x16x32_bf16 v[54:57], v[162:165], v[190:193], v[54:57]
	v_mfma_f32_16x16x32_bf16 v[50:53], v[154:157], v[186:189], v[50:53]
	v_mfma_f32_16x16x32_bf16 v[46:49], v[162:165], v[186:189], v[46:49]
	v_mfma_f32_16x16x32_bf16 v[42:45], v[154:157], v[182:185], v[42:45]
	v_mfma_f32_16x16x32_bf16 v[38:41], v[162:165], v[182:185], v[38:41]
	v_mfma_f32_16x16x32_bf16 v[34:37], v[134:137], v[178:181], v[34:37]
	v_mfma_f32_16x16x32_bf16 v[30:33], v[142:145], v[178:181], v[30:33]
	v_mfma_f32_16x16x32_bf16 v[26:29], v[134:137], v[174:177], v[26:29]
	v_mfma_f32_16x16x32_bf16 v[22:25], v[142:145], v[174:177], v[22:25]
	v_mfma_f32_16x16x32_bf16 v[18:21], v[134:137], v[170:173], v[18:21]
	v_mfma_f32_16x16x32_bf16 v[14:17], v[142:145], v[170:173], v[14:17]
	v_mfma_f32_16x16x32_bf16 v[10:13], v[134:137], v[166:169], v[10:13]
	v_mfma_f32_16x16x32_bf16 v[6:9], v[142:145], v[166:169], v[6:9]
	v_mfma_f32_16x16x32_bf16 v[34:37], v[138:141], v[194:197], v[34:37]
	v_mfma_f32_16x16x32_bf16 v[30:33], v[146:149], v[194:197], v[30:33]
	v_mfma_f32_16x16x32_bf16 v[26:29], v[138:141], v[190:193], v[26:29]
	v_mfma_f32_16x16x32_bf16 v[22:25], v[146:149], v[190:193], v[22:25]
	v_mfma_f32_16x16x32_bf16 v[18:21], v[138:141], v[186:189], v[18:21]
	v_mfma_f32_16x16x32_bf16 v[14:17], v[146:149], v[186:189], v[14:17]
	v_mfma_f32_16x16x32_bf16 v[10:13], v[138:141], v[182:185], v[10:13]
	v_mfma_f32_16x16x32_bf16 v[6:9], v[146:149], v[182:185], v[6:9]
.LBB0_1372:
	s_barrier
	v_add_u32_e32 v134, 0x18000, v226
	v_add_u32_e32 v146, 0x1c000, v226
	ds_read_b128 v[150:153], v134
	ds_read_b128 v[154:157], v134 offset:1024
	ds_read_b128 v[158:161], v134 offset:2048
	ds_read_b128 v[162:165], v134 offset:3072
	ds_read_b128 v[134:137], v146
	ds_read_b128 v[138:141], v146 offset:1024
	ds_read_b128 v[142:145], v146 offset:2048
	ds_read_b128 v[146:149], v146 offset:3072
	s_add_u32 s48, s48, 0x60000
	s_addc_u32 s49, s49, 0
	s_mov_b32 m0, s58
	v_lshl_add_u64 v[218:219], s[48:49], 0, v[198:199]
	s_waitcnt lgkmcnt(0)
	ds_read_b128 v[178:181], v227 offset:32768
	ds_read_b128 v[194:197], v227 offset:33792
	ds_read_b128 v[174:177], v227 offset:34816
	ds_read_b128 v[190:193], v227 offset:35840
	ds_read_b128 v[170:173], v227 offset:36864
	ds_read_b128 v[186:189], v227 offset:37888
	ds_read_b128 v[166:169], v227 offset:38912
	ds_read_b128 v[182:185], v227 offset:39936
	global_load_lds_dwordx4 v[218:219], off
	v_lshl_add_u64 v[218:219], s[48:49], 0, v[200:201]
	s_mov_b32 m0, s59
	s_nop 0
	global_load_lds_dwordx4 v[218:219], off
	s_waitcnt vmcnt(8)
	s_waitcnt lgkmcnt(0)
	s_barrier
	s_waitcnt lgkmcnt(0)
	v_mfma_f32_16x16x32_bf16 v[130:133], v[150:153], v[178:181], v[130:133]
	v_mfma_f32_16x16x32_bf16 v[126:129], v[158:161], v[178:181], v[126:129]
	v_mfma_f32_16x16x32_bf16 v[122:125], v[150:153], v[174:177], v[122:125]
	v_mfma_f32_16x16x32_bf16 v[118:121], v[158:161], v[174:177], v[118:121]
	v_mfma_f32_16x16x32_bf16 v[114:117], v[150:153], v[170:173], v[114:117]
	v_mfma_f32_16x16x32_bf16 v[110:113], v[158:161], v[170:173], v[110:113]
	v_mfma_f32_16x16x32_bf16 v[106:109], v[150:153], v[166:169], v[106:109]
	v_mfma_f32_16x16x32_bf16 v[102:105], v[158:161], v[166:169], v[102:105]
	v_mfma_f32_16x16x32_bf16 v[130:133], v[154:157], v[194:197], v[130:133]
	v_mfma_f32_16x16x32_bf16 v[126:129], v[162:165], v[194:197], v[126:129]
	v_mfma_f32_16x16x32_bf16 v[122:125], v[154:157], v[190:193], v[122:125]
	v_mfma_f32_16x16x32_bf16 v[118:121], v[162:165], v[190:193], v[118:121]
	v_mfma_f32_16x16x32_bf16 v[114:117], v[154:157], v[186:189], v[114:117]
	v_mfma_f32_16x16x32_bf16 v[110:113], v[162:165], v[186:189], v[110:113]
	v_mfma_f32_16x16x32_bf16 v[106:109], v[154:157], v[182:185], v[106:109]
	v_mfma_f32_16x16x32_bf16 v[102:105], v[162:165], v[182:185], v[102:105]
	v_mfma_f32_16x16x32_bf16 v[98:101], v[134:137], v[178:181], v[98:101]
	v_mfma_f32_16x16x32_bf16 v[94:97], v[142:145], v[178:181], v[94:97]
	v_mfma_f32_16x16x32_bf16 v[90:93], v[134:137], v[174:177], v[90:93]
	v_mfma_f32_16x16x32_bf16 v[86:89], v[142:145], v[174:177], v[86:89]
	v_mfma_f32_16x16x32_bf16 v[82:85], v[134:137], v[170:173], v[82:85]
	v_mfma_f32_16x16x32_bf16 v[78:81], v[142:145], v[170:173], v[78:81]
	v_mfma_f32_16x16x32_bf16 v[74:77], v[134:137], v[166:169], v[74:77]
	v_mfma_f32_16x16x32_bf16 v[70:73], v[142:145], v[166:169], v[70:73]
	v_mfma_f32_16x16x32_bf16 v[98:101], v[138:141], v[194:197], v[98:101]
	v_mfma_f32_16x16x32_bf16 v[94:97], v[146:149], v[194:197], v[94:97]
	v_mfma_f32_16x16x32_bf16 v[90:93], v[138:141], v[190:193], v[90:93]
	v_mfma_f32_16x16x32_bf16 v[86:89], v[146:149], v[190:193], v[86:89]
	v_mfma_f32_16x16x32_bf16 v[82:85], v[138:141], v[186:189], v[82:85]
	v_mfma_f32_16x16x32_bf16 v[78:81], v[146:149], v[186:189], v[78:81]
	v_mfma_f32_16x16x32_bf16 v[74:77], v[138:141], v[182:185], v[74:77]
	v_mfma_f32_16x16x32_bf16 v[70:73], v[146:149], v[182:185], v[70:73]
	s_barrier
	s_and_b64 vcc, exec, s[8:9]
	s_cbranch_vccnz .LBB0_1374
	ds_read_b128 v[178:181], v227 offset:49152
	ds_read_b128 v[194:197], v227 offset:50176
	ds_read_b128 v[174:177], v227 offset:51200
	ds_read_b128 v[190:193], v227 offset:52224
	ds_read_b128 v[170:173], v227 offset:53248
	ds_read_b128 v[186:189], v227 offset:54272
	ds_read_b128 v[166:169], v227 offset:55296
	ds_read_b128 v[182:185], v227 offset:56320
.LBB0_1374:
	s_mov_b32 m0, s62
	v_lshl_add_u64 v[208:209], v[208:209], 0, s[66:67]
	s_add_u32 s46, s46, 0x20080
	global_load_lds_dwordx4 v[208:209], off
	v_lshl_add_u64 v[208:209], v[210:211], 0, s[66:67]
	s_mov_b32 m0, s63
	s_addc_u32 s47, s47, 0
	global_load_lds_dwordx4 v[208:209], off
	v_lshl_add_u64 v[208:209], s[46:47], 0, v[0:1]
	s_mov_b32 m0, s68
	s_and_b64 vcc, exec, s[8:9]
	global_load_lds_dwordx4 v[208:209], off
	v_lshl_add_u64 v[208:209], s[46:47], 0, v[202:203]
	s_mov_b32 m0, s81
	s_nop 0
	global_load_lds_dwordx4 v[208:209], off
	v_lshl_add_u64 v[208:209], v[212:213], 0, s[66:67]
	s_mov_b32 m0, s64
	s_nop 0
	global_load_lds_dwordx4 v[208:209], off
	v_lshl_add_u64 v[208:209], v[216:217], 0, s[66:67]
	s_mov_b32 m0, s65
	s_nop 0
	global_load_lds_dwordx4 v[208:209], off
	s_waitcnt vmcnt(8)
	s_waitcnt lgkmcnt(0)
	s_barrier
	s_cbranch_vccnz .LBB0_1367
	s_waitcnt lgkmcnt(0)
	v_mfma_f32_16x16x32_bf16 v[66:69], v[150:153], v[178:181], v[66:69]
	v_mfma_f32_16x16x32_bf16 v[62:65], v[158:161], v[178:181], v[62:65]
	v_mfma_f32_16x16x32_bf16 v[58:61], v[150:153], v[174:177], v[58:61]
	v_mfma_f32_16x16x32_bf16 v[54:57], v[158:161], v[174:177], v[54:57]
	v_mfma_f32_16x16x32_bf16 v[50:53], v[150:153], v[170:173], v[50:53]
	v_mfma_f32_16x16x32_bf16 v[46:49], v[158:161], v[170:173], v[46:49]
	v_mfma_f32_16x16x32_bf16 v[42:45], v[150:153], v[166:169], v[42:45]
	v_mfma_f32_16x16x32_bf16 v[38:41], v[158:161], v[166:169], v[38:41]
	v_mfma_f32_16x16x32_bf16 v[66:69], v[154:157], v[194:197], v[66:69]
	v_mfma_f32_16x16x32_bf16 v[62:65], v[162:165], v[194:197], v[62:65]
	v_mfma_f32_16x16x32_bf16 v[58:61], v[154:157], v[190:193], v[58:61]
	v_mfma_f32_16x16x32_bf16 v[54:57], v[162:165], v[190:193], v[54:57]
	v_mfma_f32_16x16x32_bf16 v[50:53], v[154:157], v[186:189], v[50:53]
	v_mfma_f32_16x16x32_bf16 v[46:49], v[162:165], v[186:189], v[46:49]
	v_mfma_f32_16x16x32_bf16 v[42:45], v[154:157], v[182:185], v[42:45]
	v_mfma_f32_16x16x32_bf16 v[38:41], v[162:165], v[182:185], v[38:41]
	v_mfma_f32_16x16x32_bf16 v[34:37], v[134:137], v[178:181], v[34:37]
	v_mfma_f32_16x16x32_bf16 v[30:33], v[142:145], v[178:181], v[30:33]
	v_mfma_f32_16x16x32_bf16 v[26:29], v[134:137], v[174:177], v[26:29]
	v_mfma_f32_16x16x32_bf16 v[22:25], v[142:145], v[174:177], v[22:25]
	v_mfma_f32_16x16x32_bf16 v[18:21], v[134:137], v[170:173], v[18:21]
	v_mfma_f32_16x16x32_bf16 v[14:17], v[142:145], v[170:173], v[14:17]
	v_mfma_f32_16x16x32_bf16 v[10:13], v[134:137], v[166:169], v[10:13]
	v_mfma_f32_16x16x32_bf16 v[6:9], v[142:145], v[166:169], v[6:9]
	v_mfma_f32_16x16x32_bf16 v[34:37], v[138:141], v[194:197], v[34:37]
	v_mfma_f32_16x16x32_bf16 v[30:33], v[146:149], v[194:197], v[30:33]
	v_mfma_f32_16x16x32_bf16 v[26:29], v[138:141], v[190:193], v[26:29]
	v_mfma_f32_16x16x32_bf16 v[22:25], v[146:149], v[190:193], v[22:25]
	v_mfma_f32_16x16x32_bf16 v[18:21], v[138:141], v[186:189], v[18:21]
	v_mfma_f32_16x16x32_bf16 v[14:17], v[146:149], v[186:189], v[14:17]
	v_mfma_f32_16x16x32_bf16 v[10:13], v[138:141], v[182:185], v[10:13]
	v_mfma_f32_16x16x32_bf16 v[6:9], v[146:149], v[182:185], v[6:9]
	s_branch .LBB0_1367

.LBB0_1556:
	v_add_u32_e32 v54, 0x10000, v247
	ds_read_b128 v[166:169], v54
	ds_read_b128 v[170:173], v54 offset:1024
	ds_read_b128 v[174:177], v54 offset:2048
	ds_read_b128 v[178:181], v54 offset:3072
	v_add_u32_e32 v54, 0x14000, v247
	ds_read_b128 v[150:153], v54
	ds_read_b128 v[154:157], v54 offset:1024
	ds_read_b128 v[158:161], v54 offset:2048
	ds_read_b128 v[162:165], v54 offset:3072
	v_lshl_add_u64 v[54:55], s[40:41], 0, v[222:223]
	s_add_i32 m0, s26, 0xc000
	s_waitcnt lgkmcnt(0)
	ds_read_b128 v[194:197], v248
	ds_read_b128 v[210:213], v248 offset:1024
	ds_read_b128 v[190:193], v248 offset:2048
	ds_read_b128 v[206:209], v248 offset:3072
	ds_read_b128 v[186:189], v248 offset:4096
	ds_read_b128 v[202:205], v248 offset:5120
	ds_read_b128 v[182:185], v248 offset:6144
	ds_read_b128 v[198:201], v248 offset:7168
	global_load_lds_dwordx4 v[54:55], off
	v_lshl_add_u64 v[54:55], s[40:41], 0, v[224:225]
	s_add_i32 m0, s26, 0xe000
	s_nop 0
	global_load_lds_dwordx4 v[54:55], off
	s_waitcnt vmcnt(8)
	s_waitcnt lgkmcnt(0)
	s_barrier
	s_waitcnt lgkmcnt(0)
	v_mfma_f32_16x16x32_bf16 v[54:57], v[166:169], v[194:197], v[146:149]
	v_mfma_f32_16x16x32_bf16 v[58:61], v[174:177], v[194:197], v[142:145]
	v_mfma_f32_16x16x32_bf16 v[66:69], v[166:169], v[190:193], v[130:133]
	v_mfma_f32_16x16x32_bf16 v[74:77], v[174:177], v[190:193], v[126:129]
	v_mfma_f32_16x16x32_bf16 v[114:117], v[166:169], v[186:189], v[114:117]
	v_mfma_f32_16x16x32_bf16 v[110:113], v[174:177], v[186:189], v[110:113]
	v_mfma_f32_16x16x32_bf16 v[98:101], v[166:169], v[182:185], v[98:101]
	v_mfma_f32_16x16x32_bf16 v[94:97], v[174:177], v[182:185], v[94:97]
	v_mfma_f32_16x16x32_bf16 v[54:57], v[170:173], v[210:213], v[54:57]
	v_mfma_f32_16x16x32_bf16 v[58:61], v[178:181], v[210:213], v[58:61]
	v_mfma_f32_16x16x32_bf16 v[66:69], v[170:173], v[206:209], v[66:69]
	v_mfma_f32_16x16x32_bf16 v[74:77], v[178:181], v[206:209], v[74:77]
	v_mfma_f32_16x16x32_bf16 v[114:117], v[170:173], v[202:205], v[114:117]
	v_mfma_f32_16x16x32_bf16 v[110:113], v[178:181], v[202:205], v[110:113]
	v_mfma_f32_16x16x32_bf16 v[98:101], v[170:173], v[198:201], v[98:101]
	v_mfma_f32_16x16x32_bf16 v[94:97], v[178:181], v[198:201], v[94:97]
	v_mfma_f32_16x16x32_bf16 v[126:129], v[150:153], v[194:197], v[138:141]
	v_mfma_f32_16x16x32_bf16 v[138:141], v[154:157], v[210:213], v[126:129]
	v_mfma_f32_16x16x32_bf16 v[126:129], v[158:161], v[194:197], v[134:137]
	v_mfma_f32_16x16x32_bf16 v[122:125], v[150:153], v[190:193], v[122:125]
	v_mfma_f32_16x16x32_bf16 v[118:121], v[158:161], v[190:193], v[118:121]
	v_mfma_f32_16x16x32_bf16 v[106:109], v[150:153], v[186:189], v[106:109]
	v_mfma_f32_16x16x32_bf16 v[102:105], v[158:161], v[186:189], v[102:105]
	v_mfma_f32_16x16x32_bf16 v[90:93], v[150:153], v[182:185], v[90:93]
	v_mfma_f32_16x16x32_bf16 v[86:89], v[158:161], v[182:185], v[86:89]
	v_mfma_f32_16x16x32_bf16 v[134:137], v[162:165], v[210:213], v[126:129]
	v_mfma_f32_16x16x32_bf16 v[122:125], v[154:157], v[206:209], v[122:125]
	v_mfma_f32_16x16x32_bf16 v[118:121], v[162:165], v[206:209], v[118:121]
	v_mfma_f32_16x16x32_bf16 v[106:109], v[154:157], v[202:205], v[106:109]
	v_mfma_f32_16x16x32_bf16 v[102:105], v[162:165], v[202:205], v[102:105]
	v_mfma_f32_16x16x32_bf16 v[90:93], v[154:157], v[198:201], v[90:93]
	v_mfma_f32_16x16x32_bf16 v[86:89], v[162:165], v[198:201], v[86:89]
	s_barrier
	v_cndmask_b32_e64 v126, 0, 1, s[38:39]
	v_cmp_ne_u32_e64 s[0:1], 1, v126
	s_andn2_b64 vcc, exec, s[38:39]
	s_cbranch_vccnz .LBB0_1558
	ds_read_b128 v[194:197], v248 offset:16384
	ds_read_b128 v[210:213], v248 offset:17408
	ds_read_b128 v[190:193], v248 offset:18432
	ds_read_b128 v[206:209], v248 offset:19456
	ds_read_b128 v[186:189], v248 offset:20480
	ds_read_b128 v[202:205], v248 offset:21504
	ds_read_b128 v[182:185], v248 offset:22528
	ds_read_b128 v[198:201], v248 offset:23552
.LBB0_1558:
	s_add_u32 s42, s40, 0xfffc0080
	s_addc_u32 s43, s41, -1
	s_cmp_eq_u32 s90, 12
	s_cselect_b32 s45, s74, s43
	s_cselect_b32 s44, s75, s42
	s_cselect_b32 s43, s11, s88
	s_cselect_b32 s42, s81, s83
	s_mov_b32 m0, s27
	v_lshl_add_u64 v[226:227], s[42:43], 0, v[0:1]
	s_add_u32 vcc_lo, s42, 0x40000
	global_load_lds_dwordx4 v[226:227], off
	v_lshl_add_u64 v[228:229], s[42:43], 0, v[220:221]
	s_mov_b32 m0, s37
	s_addc_u32 vcc_hi, s43, 0
	global_load_lds_dwordx4 v[228:229], off
	v_lshl_add_u64 v[126:127], vcc, 0, v[0:1]
	s_mov_b32 m0, s47
	v_lshl_add_u64 v[230:231], s[44:45], 0, v[216:217]
	global_load_lds_dwordx4 v[126:127], off
	v_lshl_add_u64 v[126:127], vcc, 0, v[220:221]
	s_mov_b32 m0, s48
	v_lshl_add_u64 v[232:233], s[44:45], 0, v[218:219]
	global_load_lds_dwordx4 v[126:127], off
	s_mov_b32 m0, s26
	s_and_b64 vcc, exec, s[0:1]
	global_load_lds_dwordx4 v[230:231], off
	s_mov_b32 m0, s49
	s_nop 0
	global_load_lds_dwordx4 v[232:233], off
	s_waitcnt vmcnt(8)
	s_waitcnt lgkmcnt(0)
	s_barrier
	s_cbranch_vccnz .LBB0_1560
	s_waitcnt lgkmcnt(0)
	v_mfma_f32_16x16x32_bf16 v[82:85], v[166:169], v[194:197], v[82:85]
	v_mfma_f32_16x16x32_bf16 v[78:81], v[174:177], v[194:197], v[78:81]
	v_mfma_f32_16x16x32_bf16 v[50:53], v[166:169], v[190:193], v[50:53]
	v_mfma_f32_16x16x32_bf16 v[46:49], v[174:177], v[190:193], v[46:49]
	v_mfma_f32_16x16x32_bf16 v[34:37], v[166:169], v[186:189], v[34:37]
	v_mfma_f32_16x16x32_bf16 v[30:33], v[174:177], v[186:189], v[30:33]
	v_mfma_f32_16x16x32_bf16 v[18:21], v[166:169], v[182:185], v[18:21]
	v_mfma_f32_16x16x32_bf16 v[14:17], v[174:177], v[182:185], v[14:17]
	v_mfma_f32_16x16x32_bf16 v[82:85], v[170:173], v[210:213], v[82:85]
	v_mfma_f32_16x16x32_bf16 v[78:81], v[178:181], v[210:213], v[78:81]
	v_mfma_f32_16x16x32_bf16 v[50:53], v[170:173], v[206:209], v[50:53]
	v_mfma_f32_16x16x32_bf16 v[46:49], v[178:181], v[206:209], v[46:49]
	v_mfma_f32_16x16x32_bf16 v[34:37], v[170:173], v[202:205], v[34:37]
	v_mfma_f32_16x16x32_bf16 v[30:33], v[178:181], v[202:205], v[30:33]
	v_mfma_f32_16x16x32_bf16 v[18:21], v[170:173], v[198:201], v[18:21]
	v_mfma_f32_16x16x32_bf16 v[14:17], v[178:181], v[198:201], v[14:17]
	v_mfma_f32_16x16x32_bf16 v[70:73], v[150:153], v[194:197], v[70:73]
	v_mfma_f32_16x16x32_bf16 v[62:65], v[158:161], v[194:197], v[62:65]
	v_mfma_f32_16x16x32_bf16 v[42:45], v[150:153], v[190:193], v[42:45]
	v_mfma_f32_16x16x32_bf16 v[38:41], v[158:161], v[190:193], v[38:41]
	v_mfma_f32_16x16x32_bf16 v[26:29], v[150:153], v[186:189], v[26:29]
	v_mfma_f32_16x16x32_bf16 v[22:25], v[158:161], v[186:189], v[22:25]
	v_mfma_f32_16x16x32_bf16 v[10:13], v[150:153], v[182:185], v[10:13]
	v_mfma_f32_16x16x32_bf16 v[6:9], v[158:161], v[182:185], v[6:9]
	v_mfma_f32_16x16x32_bf16 v[70:73], v[154:157], v[210:213], v[70:73]
	v_mfma_f32_16x16x32_bf16 v[62:65], v[162:165], v[210:213], v[62:65]
	v_mfma_f32_16x16x32_bf16 v[42:45], v[154:157], v[206:209], v[42:45]
	v_mfma_f32_16x16x32_bf16 v[38:41], v[162:165], v[206:209], v[38:41]
	v_mfma_f32_16x16x32_bf16 v[26:29], v[154:157], v[202:205], v[26:29]
	v_mfma_f32_16x16x32_bf16 v[22:25], v[162:165], v[202:205], v[22:25]
	v_mfma_f32_16x16x32_bf16 v[10:13], v[154:157], v[198:201], v[10:13]
	v_mfma_f32_16x16x32_bf16 v[6:9], v[162:165], v[198:201], v[6:9]
.LBB0_1560:
	s_barrier
	v_add_u32_e32 v126, 0x18000, v247
	ds_read_b128 v[166:169], v126
	ds_read_b128 v[170:173], v126 offset:1024
	ds_read_b128 v[174:177], v126 offset:2048
	ds_read_b128 v[178:181], v126 offset:3072
	v_add_u32_e32 v126, 0x1c000, v247
	ds_read_b128 v[150:153], v126
	ds_read_b128 v[154:157], v126 offset:1024
	ds_read_b128 v[158:161], v126 offset:2048
	ds_read_b128 v[162:165], v126 offset:3072
	s_add_u32 s44, s44, 0x40000
	s_addc_u32 s45, s45, 0
	s_mov_b32 m0, s50
	v_lshl_add_u64 v[126:127], s[44:45], 0, v[216:217]
	s_waitcnt lgkmcnt(0)
	ds_read_b128 v[194:197], v248 offset:32768
	ds_read_b128 v[210:213], v248 offset:33792
	ds_read_b128 v[190:193], v248 offset:34816
	ds_read_b128 v[206:209], v248 offset:35840
	ds_read_b128 v[186:189], v248 offset:36864
	ds_read_b128 v[202:205], v248 offset:37888
	ds_read_b128 v[182:185], v248 offset:38912
	ds_read_b128 v[198:201], v248 offset:39936
	global_load_lds_dwordx4 v[126:127], off
	v_lshl_add_u64 v[126:127], s[44:45], 0, v[218:219]
	s_mov_b32 m0, s51
	s_nop 0
	global_load_lds_dwordx4 v[126:127], off
	s_waitcnt vmcnt(8)
	s_waitcnt lgkmcnt(0)
	s_barrier
	s_waitcnt lgkmcnt(0)
	v_mfma_f32_16x16x32_bf16 v[54:57], v[166:169], v[194:197], v[54:57]
	v_mfma_f32_16x16x32_bf16 v[146:149], v[170:173], v[210:213], v[54:57]
	v_mfma_f32_16x16x32_bf16 v[54:57], v[174:177], v[194:197], v[58:61]
	v_mfma_f32_16x16x32_bf16 v[142:145], v[178:181], v[210:213], v[54:57]
	v_mfma_f32_16x16x32_bf16 v[54:57], v[166:169], v[190:193], v[66:69]
	v_mfma_f32_16x16x32_bf16 v[130:133], v[170:173], v[206:209], v[54:57]
	v_mfma_f32_16x16x32_bf16 v[54:57], v[174:177], v[190:193], v[74:77]
	v_mfma_f32_16x16x32_bf16 v[126:129], v[178:181], v[206:209], v[54:57]
	v_mfma_f32_16x16x32_bf16 v[54:57], v[166:169], v[186:189], v[114:117]
	v_mfma_f32_16x16x32_bf16 v[114:117], v[170:173], v[202:205], v[54:57]
	v_mfma_f32_16x16x32_bf16 v[54:57], v[174:177], v[186:189], v[110:113]
	v_mfma_f32_16x16x32_bf16 v[110:113], v[178:181], v[202:205], v[54:57]
	v_mfma_f32_16x16x32_bf16 v[54:57], v[166:169], v[182:185], v[98:101]
	v_mfma_f32_16x16x32_bf16 v[98:101], v[170:173], v[198:201], v[54:57]
	v_mfma_f32_16x16x32_bf16 v[54:57], v[174:177], v[182:185], v[94:97]
	v_mfma_f32_16x16x32_bf16 v[94:97], v[178:181], v[198:201], v[54:57]
	v_mfma_f32_16x16x32_bf16 v[54:57], v[150:153], v[194:197], v[138:141]
	v_mfma_f32_16x16x32_bf16 v[138:141], v[154:157], v[210:213], v[54:57]
	v_mfma_f32_16x16x32_bf16 v[54:57], v[158:161], v[194:197], v[134:137]
	v_mfma_f32_16x16x32_bf16 v[134:137], v[162:165], v[210:213], v[54:57]
	v_mfma_f32_16x16x32_bf16 v[54:57], v[150:153], v[190:193], v[122:125]
	v_mfma_f32_16x16x32_bf16 v[122:125], v[154:157], v[206:209], v[54:57]
	v_mfma_f32_16x16x32_bf16 v[54:57], v[158:161], v[190:193], v[118:121]
	v_mfma_f32_16x16x32_bf16 v[118:121], v[162:165], v[206:209], v[54:57]
	v_mfma_f32_16x16x32_bf16 v[54:57], v[150:153], v[186:189], v[106:109]
	v_mfma_f32_16x16x32_bf16 v[106:109], v[154:157], v[202:205], v[54:57]
	v_mfma_f32_16x16x32_bf16 v[54:57], v[158:161], v[186:189], v[102:105]
	v_mfma_f32_16x16x32_bf16 v[102:105], v[162:165], v[202:205], v[54:57]
	v_mfma_f32_16x16x32_bf16 v[54:57], v[150:153], v[182:185], v[90:93]
	v_mfma_f32_16x16x32_bf16 v[90:93], v[154:157], v[198:201], v[54:57]
	v_mfma_f32_16x16x32_bf16 v[54:57], v[158:161], v[182:185], v[86:89]
	v_mfma_f32_16x16x32_bf16 v[86:89], v[162:165], v[198:201], v[54:57]
	s_barrier
	s_and_b64 vcc, exec, s[0:1]
	s_cbranch_vccnz .LBB0_1562
	ds_read_b128 v[194:197], v248 offset:49152
	ds_read_b128 v[210:213], v248 offset:50176
	ds_read_b128 v[190:193], v248 offset:51200
	ds_read_b128 v[206:209], v248 offset:52224
	ds_read_b128 v[186:189], v248 offset:53248
	ds_read_b128 v[202:205], v248 offset:54272
	ds_read_b128 v[182:185], v248 offset:55296
	ds_read_b128 v[198:201], v248 offset:56320
.LBB0_1562:
	s_mov_b32 m0, s56
	s_nop 1
	v_lshl_add_u64 v[54:55], v[226:227], 0, s[66:67]
	s_add_u32 s42, s42, 0x40080
	global_load_lds_dwordx4 v[54:55], off
	v_lshl_add_u64 v[54:55], v[228:229], 0, s[66:67]
	s_mov_b32 m0, s57
	s_addc_u32 s43, s43, 0
	global_load_lds_dwordx4 v[54:55], off
	v_lshl_add_u64 v[54:55], s[42:43], 0, v[0:1]
	s_mov_b32 m0, s60
	s_and_b64 vcc, exec, s[0:1]
	global_load_lds_dwordx4 v[54:55], off
	v_lshl_add_u64 v[54:55], s[42:43], 0, v[220:221]
	s_mov_b32 m0, s61
	s_nop 0
	global_load_lds_dwordx4 v[54:55], off
	v_lshl_add_u64 v[54:55], v[230:231], 0, s[66:67]
	s_mov_b32 m0, s58
	s_nop 0
	global_load_lds_dwordx4 v[54:55], off
	v_lshl_add_u64 v[54:55], v[232:233], 0, s[66:67]
	s_mov_b32 m0, s59
	s_nop 0
	global_load_lds_dwordx4 v[54:55], off
	s_waitcnt vmcnt(8)
	s_waitcnt lgkmcnt(0)
	s_barrier
	s_cbranch_vccnz .LBB0_1555
	s_waitcnt lgkmcnt(0)
	v_mfma_f32_16x16x32_bf16 v[54:57], v[166:169], v[194:197], v[82:85]
	v_mfma_f32_16x16x32_bf16 v[82:85], v[170:173], v[210:213], v[54:57]
	v_mfma_f32_16x16x32_bf16 v[54:57], v[174:177], v[194:197], v[78:81]
	v_mfma_f32_16x16x32_bf16 v[50:53], v[166:169], v[190:193], v[50:53]
	v_mfma_f32_16x16x32_bf16 v[46:49], v[174:177], v[190:193], v[46:49]
	v_mfma_f32_16x16x32_bf16 v[34:37], v[166:169], v[186:189], v[34:37]
	v_mfma_f32_16x16x32_bf16 v[30:33], v[174:177], v[186:189], v[30:33]
	v_mfma_f32_16x16x32_bf16 v[18:21], v[166:169], v[182:185], v[18:21]
	v_mfma_f32_16x16x32_bf16 v[14:17], v[174:177], v[182:185], v[14:17]
	v_mfma_f32_16x16x32_bf16 v[78:81], v[178:181], v[210:213], v[54:57]
	v_mfma_f32_16x16x32_bf16 v[50:53], v[170:173], v[206:209], v[50:53]
	v_mfma_f32_16x16x32_bf16 v[46:49], v[178:181], v[206:209], v[46:49]
	v_mfma_f32_16x16x32_bf16 v[34:37], v[170:173], v[202:205], v[34:37]
	v_mfma_f32_16x16x32_bf16 v[30:33], v[178:181], v[202:205], v[30:33]
	v_mfma_f32_16x16x32_bf16 v[18:21], v[170:173], v[198:201], v[18:21]
	v_mfma_f32_16x16x32_bf16 v[14:17], v[178:181], v[198:201], v[14:17]
	v_mfma_f32_16x16x32_bf16 v[54:57], v[150:153], v[194:197], v[70:73]
	v_mfma_f32_16x16x32_bf16 v[70:73], v[154:157], v[210:213], v[54:57]
	v_mfma_f32_16x16x32_bf16 v[54:57], v[158:161], v[194:197], v[62:65]
	v_mfma_f32_16x16x32_bf16 v[42:45], v[150:153], v[190:193], v[42:45]
	v_mfma_f32_16x16x32_bf16 v[38:41], v[158:161], v[190:193], v[38:41]
	v_mfma_f32_16x16x32_bf16 v[26:29], v[150:153], v[186:189], v[26:29]
	v_mfma_f32_16x16x32_bf16 v[22:25], v[158:161], v[186:189], v[22:25]
	v_mfma_f32_16x16x32_bf16 v[10:13], v[150:153], v[182:185], v[10:13]
	v_mfma_f32_16x16x32_bf16 v[6:9], v[158:161], v[182:185], v[6:9]
	v_mfma_f32_16x16x32_bf16 v[62:65], v[162:165], v[210:213], v[54:57]
	v_mfma_f32_16x16x32_bf16 v[42:45], v[154:157], v[206:209], v[42:45]
	v_mfma_f32_16x16x32_bf16 v[38:41], v[162:165], v[206:209], v[38:41]
	v_mfma_f32_16x16x32_bf16 v[26:29], v[154:157], v[202:205], v[26:29]
	v_mfma_f32_16x16x32_bf16 v[22:25], v[162:165], v[202:205], v[22:25]
	v_mfma_f32_16x16x32_bf16 v[10:13], v[154:157], v[198:201], v[10:13]
	v_mfma_f32_16x16x32_bf16 v[6:9], v[162:165], v[198:201], v[6:9]
	s_branch .LBB0_1555

.Lrw_done_g1_0:
	s_waitcnt lgkmcnt(0)
	v_mov_b32_e32 v169, v1
	s_barrier
	s_waitcnt lgkmcnt(0)
	v_mfma_scale_f32_16x16x128_f8f6f4 v[150:153], v[26:33], v[198:205], 0, v234, v235 op_sel_hi:[0,0,0]
	v_mfma_scale_f32_16x16x128_f8f6f4 v[146:149], v[18:25], v[198:205], 0, v234, v235 op_sel_hi:[0,0,0]
	v_mfma_scale_f32_16x16x128_f8f6f4 v[142:145], v[26:33], v[206:213], 0, v234, v235 op_sel_hi:[0,0,0]
	v_mfma_scale_f32_16x16x128_f8f6f4 v[138:141], v[18:25], v[206:213], 0, v234, v235 op_sel_hi:[0,0,0]
	v_mfma_scale_f32_16x16x128_f8f6f4 v[134:137], v[26:33], v[216:223], 0, v234, v235 op_sel_hi:[0,0,0]
	v_mfma_scale_f32_16x16x128_f8f6f4 v[130:133], v[18:25], v[216:223], 0, v234, v235 op_sel_hi:[0,0,0]
	v_mfma_scale_f32_16x16x128_f8f6f4 v[126:129], v[26:33], v[224:231], 0, v234, v235 op_sel_hi:[0,0,0]
	v_mfma_scale_f32_16x16x128_f8f6f4 v[122:125], v[18:25], v[224:231], 0, v234, v235 op_sel_hi:[0,0,0]
	v_mfma_scale_f32_16x16x128_f8f6f4 v[118:121], v[10:17], v[198:205], 0, v234, v235 op_sel_hi:[0,0,0]
	v_mfma_scale_f32_16x16x128_f8f6f4 v[114:117], v[2:9], v[198:205], 0, v234, v235 op_sel_hi:[0,0,0]
	v_mfma_scale_f32_16x16x128_f8f6f4 v[110:113], v[10:17], v[206:213], 0, v234, v235 op_sel_hi:[0,0,0]
	v_mfma_scale_f32_16x16x128_f8f6f4 v[106:109], v[2:9], v[206:213], 0, v234, v235 op_sel_hi:[0,0,0]
	v_mfma_scale_f32_16x16x128_f8f6f4 v[102:105], v[10:17], v[216:223], 0, v234, v235 op_sel_hi:[0,0,0]
	v_mfma_scale_f32_16x16x128_f8f6f4 v[98:101], v[2:9], v[216:223], 0, v234, v235 op_sel_hi:[0,0,0]
	v_mfma_scale_f32_16x16x128_f8f6f4 v[94:97], v[10:17], v[224:231], 0, v234, v235 op_sel_hi:[0,0,0]
	v_mfma_scale_f32_16x16x128_f8f6f4 v[90:93], v[2:9], v[224:231], 0, v234, v235 op_sel_hi:[0,0,0]
	s_barrier
	v_lshl_add_u64 v[170:171], s[4:5], 0, v[162:163]
	s_mov_b64 s[54:55], 0x100
	s_mov_b32 m0, s68
	v_lshl_add_u64 v[172:173], v[170:171], 0, s[54:55]
	ds_read_b128 v[198:201], v192 offset:16384
	ds_read_b128 v[202:205], v192 offset:17408
	ds_read_b128 v[206:209], v192 offset:18432
	ds_read_b128 v[210:213], v192 offset:19456
	ds_read_b128 v[216:219], v192 offset:20480
	ds_read_b128 v[220:223], v192 offset:21504
	ds_read_b128 v[224:227], v192 offset:22528
	ds_read_b128 v[228:231], v192 offset:23552
	global_load_lds_dwordx4 v[172:173], off
	v_lshl_add_u64 v[172:173], s[4:5], 0, v[164:165]
	v_lshl_add_u64 v[232:233], v[172:173], 0, s[54:55]
	s_add_u32 s54, s4, 0x20100
	s_mov_b32 m0, s60
	s_addc_u32 s55, s5, 0
	global_load_lds_dwordx4 v[232:233], off
	v_lshl_add_u64 v[232:233], s[54:55], 0, v[162:163]
	s_mov_b32 m0, s61
	v_lshlrev_b32_e32 v0, 10, v195
	global_load_lds_dwordx4 v[232:233], off
	v_lshl_add_u64 v[232:233], s[54:55], 0, v[164:165]
	s_mov_b32 m0, s62
	v_and_or_b32 v0, v0, s82, v174
	global_load_lds_dwordx4 v[232:233], off
	v_bfe_u32 v197, v195, 16, 16
	s_mov_b32 m0, s65
	v_lshl_add_u32 v197, v197, 10, v175
	global_load_lds_dwordx4 v0, s[34:35]
	s_mov_b32 m0, s63
	s_nop 0
	global_load_lds_dwordx4 v197, s[34:35]
	s_cmp_eq_u32 s23, 0
	s_cbranch_scc1 .Lrw_first_g1_1
	s_waitcnt vmcnt(12)
	s_branch .Lrw_done_g1_1

.Lrw_done_g1_1:
	s_waitcnt lgkmcnt(0)
	s_barrier
	s_waitcnt lgkmcnt(0)
	v_mfma_scale_f32_16x16x128_f8f6f4 v[86:89], v[26:33], v[198:205], 0, v234, v235 op_sel_hi:[0,0,0]
	v_mfma_scale_f32_16x16x128_f8f6f4 v[82:85], v[18:25], v[198:205], 0, v234, v235 op_sel_hi:[0,0,0]
	v_mfma_scale_f32_16x16x128_f8f6f4 v[78:81], v[26:33], v[206:213], 0, v234, v235 op_sel_hi:[0,0,0]
	v_mfma_scale_f32_16x16x128_f8f6f4 v[74:77], v[18:25], v[206:213], 0, v234, v235 op_sel_hi:[0,0,0]
	v_mfma_scale_f32_16x16x128_f8f6f4 v[70:73], v[26:33], v[216:223], 0, v234, v235 op_sel_hi:[0,0,0]
	v_mfma_scale_f32_16x16x128_f8f6f4 v[66:69], v[18:25], v[216:223], 0, v234, v235 op_sel_hi:[0,0,0]
	v_mfma_scale_f32_16x16x128_f8f6f4 v[62:65], v[26:33], v[224:231], 0, v234, v235 op_sel_hi:[0,0,0]
	v_mfma_scale_f32_16x16x128_f8f6f4 v[58:61], v[18:25], v[224:231], 0, v234, v235 op_sel_hi:[0,0,0]
	v_mfma_scale_f32_16x16x128_f8f6f4 v[54:57], v[10:17], v[198:205], 0, v234, v235 op_sel_hi:[0,0,0]
	v_mfma_scale_f32_16x16x128_f8f6f4 v[50:53], v[2:9], v[198:205], 0, v234, v235 op_sel_hi:[0,0,0]
	v_mfma_scale_f32_16x16x128_f8f6f4 v[46:49], v[10:17], v[206:213], 0, v234, v235 op_sel_hi:[0,0,0]
	v_mfma_scale_f32_16x16x128_f8f6f4 v[42:45], v[2:9], v[206:213], 0, v234, v235 op_sel_hi:[0,0,0]
	v_mfma_scale_f32_16x16x128_f8f6f4 v[38:41], v[10:17], v[216:223], 0, v234, v235 op_sel_hi:[0,0,0]
	v_mfma_scale_f32_16x16x128_f8f6f4 v[34:37], v[2:9], v[216:223], 0, v234, v235 op_sel_hi:[0,0,0]
	v_mfma_scale_f32_16x16x128_f8f6f4 v[154:157], v[10:17], v[224:231], 0, v234, v235 op_sel_hi:[0,0,0]
	v_mfma_scale_f32_16x16x128_f8f6f4 v[158:161], v[2:9], v[224:231], 0, v234, v235 op_sel_hi:[0,0,0]
	s_barrier
	ds_read_b128 v[18:21], v184
	ds_read_b128 v[22:25], v185
	ds_read_b128 v[26:29], v186
	ds_read_b128 v[30:33], v187
	ds_read_b128 v[2:5], v188
	ds_read_b128 v[6:9], v189
	ds_read_b128 v[10:13], v190
	ds_read_b128 v[14:17], v191
	s_mov_b32 m0, s10
	ds_read_b128 v[198:201], v192 offset:32768
	ds_read_b128 v[202:205], v192 offset:33792
	ds_read_b128 v[206:209], v192 offset:34816
	ds_read_b128 v[210:213], v192 offset:35840
	ds_read_b128 v[216:219], v192 offset:36864
	ds_read_b128 v[220:223], v192 offset:37888
	ds_read_b128 v[224:227], v192 offset:38912
	ds_read_b128 v[228:231], v192 offset:39936
	global_load_lds_dwordx4 v166, s[34:35]
	s_mov_b32 m0, s11
	s_nop 0
	global_load_lds_dwordx4 v168, s[34:35]
	s_waitcnt vmcnt(8)
	s_waitcnt lgkmcnt(0)
	s_barrier
	s_waitcnt lgkmcnt(0)
	v_mfma_scale_f32_16x16x128_f8f6f4 v[150:153], v[18:25], v[198:205], v[150:153], v234, v235 op_sel_hi:[0,0,0]
	v_mfma_scale_f32_16x16x128_f8f6f4 v[146:149], v[26:33], v[198:205], v[146:149], v234, v235 op_sel_hi:[0,0,0]
	v_mfma_scale_f32_16x16x128_f8f6f4 v[142:145], v[18:25], v[206:213], v[142:145], v234, v235 op_sel_hi:[0,0,0]
	v_mfma_scale_f32_16x16x128_f8f6f4 v[138:141], v[26:33], v[206:213], v[138:141], v234, v235 op_sel_hi:[0,0,0]
	v_mfma_scale_f32_16x16x128_f8f6f4 v[134:137], v[18:25], v[216:223], v[134:137], v234, v235 op_sel_hi:[0,0,0]
	v_mfma_scale_f32_16x16x128_f8f6f4 v[130:133], v[26:33], v[216:223], v[130:133], v234, v235 op_sel_hi:[0,0,0]
	v_mfma_scale_f32_16x16x128_f8f6f4 v[126:129], v[18:25], v[224:231], v[126:129], v234, v235 op_sel_hi:[0,0,0]
	v_mfma_scale_f32_16x16x128_f8f6f4 v[122:125], v[26:33], v[224:231], v[122:125], v234, v235 op_sel_hi:[0,0,0]
	v_mfma_scale_f32_16x16x128_f8f6f4 v[118:121], v[2:9], v[198:205], v[118:121], v234, v235 op_sel_hi:[0,0,0]
	v_mfma_scale_f32_16x16x128_f8f6f4 v[114:117], v[10:17], v[198:205], v[114:117], v234, v235 op_sel_hi:[0,0,0]
	v_mfma_scale_f32_16x16x128_f8f6f4 v[110:113], v[2:9], v[206:213], v[110:113], v234, v235 op_sel_hi:[0,0,0]
	v_mfma_scale_f32_16x16x128_f8f6f4 v[106:109], v[10:17], v[206:213], v[106:109], v234, v235 op_sel_hi:[0,0,0]
	v_mfma_scale_f32_16x16x128_f8f6f4 v[102:105], v[2:9], v[216:223], v[102:105], v234, v235 op_sel_hi:[0,0,0]
	v_mfma_scale_f32_16x16x128_f8f6f4 v[98:101], v[10:17], v[216:223], v[98:101], v234, v235 op_sel_hi:[0,0,0]
	v_mfma_scale_f32_16x16x128_f8f6f4 v[94:97], v[2:9], v[224:231], v[94:97], v234, v235 op_sel_hi:[0,0,0]
	v_mfma_scale_f32_16x16x128_f8f6f4 v[90:93], v[10:17], v[224:231], v[90:93], v234, v235 op_sel_hi:[0,0,0]
	s_barrier
	s_mov_b64 s[54:55], 0x180
	s_mov_b32 m0, s64
	v_lshl_add_u64 v[170:171], v[170:171], 0, s[54:55]
	ds_read_b128 v[198:201], v192 offset:49152
	ds_read_b128 v[202:205], v192 offset:50176
	ds_read_b128 v[206:209], v192 offset:51200
	ds_read_b128 v[210:213], v192 offset:52224
	ds_read_b128 v[216:219], v192 offset:53248
	ds_read_b128 v[220:223], v192 offset:54272
	ds_read_b128 v[224:227], v192 offset:55296
	ds_read_b128 v[228:231], v192 offset:56320
	global_load_lds_dwordx4 v[170:171], off
	v_lshl_add_u64 v[170:171], v[172:173], 0, s[54:55]
	s_add_u32 s54, s4, 0x20180
	s_mov_b32 m0, s81
	s_addc_u32 s55, s5, 0
	global_load_lds_dwordx4 v[170:171], off
	v_lshl_add_u64 v[170:171], s[54:55], 0, v[162:163]
	s_mov_b32 m0, s49
	s_nop 0
	global_load_lds_dwordx4 v[170:171], off
	v_lshl_add_u64 v[170:171], s[54:55], 0, v[164:165]
	s_mov_b32 m0, s30
	s_nop 0
	global_load_lds_dwordx4 v[170:171], off
	s_mov_b32 m0, s6
	s_nop 0
	global_load_lds_dwordx4 v0, s[36:37]
	s_mov_b32 m0, s7
	s_nop 0
	global_load_lds_dwordx4 v197, s[36:37]
	s_waitcnt vmcnt(8)
	s_waitcnt lgkmcnt(0)
	s_barrier
	s_waitcnt lgkmcnt(0)
	v_mfma_scale_f32_16x16x128_f8f6f4 v[86:89], v[18:25], v[198:205], v[86:89], v234, v235 op_sel_hi:[0,0,0]
	v_mfma_scale_f32_16x16x128_f8f6f4 v[82:85], v[26:33], v[198:205], v[82:85], v234, v235 op_sel_hi:[0,0,0]
	v_mfma_scale_f32_16x16x128_f8f6f4 v[78:81], v[18:25], v[206:213], v[78:81], v234, v235 op_sel_hi:[0,0,0]
	v_mfma_scale_f32_16x16x128_f8f6f4 v[74:77], v[26:33], v[206:213], v[74:77], v234, v235 op_sel_hi:[0,0,0]
	v_mfma_scale_f32_16x16x128_f8f6f4 v[70:73], v[18:25], v[216:223], v[70:73], v234, v235 op_sel_hi:[0,0,0]
	v_mfma_scale_f32_16x16x128_f8f6f4 v[66:69], v[26:33], v[216:223], v[66:69], v234, v235 op_sel_hi:[0,0,0]
	v_mfma_scale_f32_16x16x128_f8f6f4 v[62:65], v[18:25], v[224:231], v[62:65], v234, v235 op_sel_hi:[0,0,0]
	v_mfma_scale_f32_16x16x128_f8f6f4 v[58:61], v[26:33], v[224:231], v[58:61], v234, v235 op_sel_hi:[0,0,0]
	v_mfma_scale_f32_16x16x128_f8f6f4 v[54:57], v[2:9], v[198:205], v[54:57], v234, v235 op_sel_hi:[0,0,0]
	v_mfma_scale_f32_16x16x128_f8f6f4 v[50:53], v[10:17], v[198:205], v[50:53], v234, v235 op_sel_hi:[0,0,0]
	v_mfma_scale_f32_16x16x128_f8f6f4 v[46:49], v[2:9], v[206:213], v[46:49], v234, v235 op_sel_hi:[0,0,0]
	v_mfma_scale_f32_16x16x128_f8f6f4 v[42:45], v[10:17], v[206:213], v[42:45], v234, v235 op_sel_hi:[0,0,0]
	v_mfma_scale_f32_16x16x128_f8f6f4 v[38:41], v[2:9], v[216:223], v[38:41], v234, v235 op_sel_hi:[0,0,0]
	v_mfma_scale_f32_16x16x128_f8f6f4 v[34:37], v[10:17], v[216:223], v[34:37], v234, v235 op_sel_hi:[0,0,0]
	v_mfma_scale_f32_16x16x128_f8f6f4 v[154:157], v[2:9], v[224:231], v[154:157], v234, v235 op_sel_hi:[0,0,0]
	v_mfma_scale_f32_16x16x128_f8f6f4 v[158:161], v[10:17], v[224:231], v[158:161], v234, v235 op_sel_hi:[0,0,0]
	s_barrier
	s_add_u32 s43, s4, 0x200
	s_addc_u32 s45, s5, 0
	s_mov_b32 s74, 0
	s_mov_b64 s[54:55], s[36:37]
	s_branch .LBB0_2003
.LBB0_2002:
	ds_read_b128 v[2:5], v183
	ds_read_b128 v[6:9], v182
	ds_read_b128 v[10:13], v181
	ds_read_b128 v[14:17], v180
	ds_read_b128 v[26:29], v179
	ds_read_b128 v[30:33], v178
	ds_read_b128 v[198:201], v177
	ds_read_b128 v[202:205], v176
	s_add_u32 s58, s54, 0x80
	s_addc_u32 s59, s55, 0
	s_and_b64 s[56:57], s[4:5], exec
	s_cselect_b32 s59, s9, s59
	s_cselect_b32 s58, s8, s58
	s_cselect_b32 s57, s47, s45
	s_cselect_b32 s56, s46, s43
	s_mov_b32 m0, s27
	v_lshl_add_u64 v[170:171], s[54:55], 0, v[166:167]
	ds_read_b128 v[18:21], v192
	ds_read_b128 v[22:25], v192 offset:1024
	ds_read_b128 v[206:209], v192 offset:2048
	ds_read_b128 v[210:213], v192 offset:3072
	ds_read_b128 v[216:219], v192 offset:4096
	ds_read_b128 v[220:223], v192 offset:5120
	ds_read_b128 v[224:227], v192 offset:6144
	ds_read_b128 v[228:231], v192 offset:7168
	global_load_lds_dwordx4 v[170:171], off
	v_lshl_add_u64 v[170:171], s[54:55], 0, v[168:169]
	s_mov_b32 m0, s41
	s_nop 0
	global_load_lds_dwordx4 v[170:171], off
	s_waitcnt vmcnt(8)
	s_waitcnt lgkmcnt(0)
	s_barrier
	s_waitcnt lgkmcnt(0)
	v_mfma_scale_f32_16x16x128_f8f6f4 v[150:153], v[2:9], v[18:25], v[150:153], v234, v235 op_sel_hi:[0,0,0]
	v_mfma_scale_f32_16x16x128_f8f6f4 v[146:149], v[10:17], v[18:25], v[146:149], v234, v235 op_sel_hi:[0,0,0]
	v_mfma_scale_f32_16x16x128_f8f6f4 v[142:145], v[2:9], v[206:213], v[142:145], v234, v235 op_sel_hi:[0,0,0]
	v_mfma_scale_f32_16x16x128_f8f6f4 v[138:141], v[10:17], v[206:213], v[138:141], v234, v235 op_sel_hi:[0,0,0]
	v_mfma_scale_f32_16x16x128_f8f6f4 v[134:137], v[2:9], v[216:223], v[134:137], v234, v235 op_sel_hi:[0,0,0]
	v_mfma_scale_f32_16x16x128_f8f6f4 v[130:133], v[10:17], v[216:223], v[130:133], v234, v235 op_sel_hi:[0,0,0]
	v_mfma_scale_f32_16x16x128_f8f6f4 v[126:129], v[2:9], v[224:231], v[126:129], v234, v235 op_sel_hi:[0,0,0]
	v_mfma_scale_f32_16x16x128_f8f6f4 v[122:125], v[10:17], v[224:231], v[122:125], v234, v235 op_sel_hi:[0,0,0]
	v_mfma_scale_f32_16x16x128_f8f6f4 v[118:121], v[26:33], v[18:25], v[118:121], v234, v235 op_sel_hi:[0,0,0]
	v_mfma_scale_f32_16x16x128_f8f6f4 v[114:117], v[198:205], v[18:25], v[114:117], v234, v235 op_sel_hi:[0,0,0]
	v_mfma_scale_f32_16x16x128_f8f6f4 v[110:113], v[26:33], v[206:213], v[110:113], v234, v235 op_sel_hi:[0,0,0]
	v_mfma_scale_f32_16x16x128_f8f6f4 v[106:109], v[198:205], v[206:213], v[106:109], v234, v235 op_sel_hi:[0,0,0]
	v_mfma_scale_f32_16x16x128_f8f6f4 v[102:105], v[26:33], v[216:223], v[102:105], v234, v235 op_sel_hi:[0,0,0]
	v_mfma_scale_f32_16x16x128_f8f6f4 v[98:101], v[198:205], v[216:223], v[98:101], v234, v235 op_sel_hi:[0,0,0]
	v_mfma_scale_f32_16x16x128_f8f6f4 v[94:97], v[26:33], v[224:231], v[94:97], v234, v235 op_sel_hi:[0,0,0]
	v_mfma_scale_f32_16x16x128_f8f6f4 v[90:93], v[198:205], v[224:231], v[90:93], v234, v235 op_sel_hi:[0,0,0]
	s_barrier
	s_mov_b32 m0, s68
	v_lshl_add_u64 v[18:19], s[56:57], 0, v[162:163]
	s_add_u32 vcc_lo, s56, 0x20000
	ds_read_b128 v[206:209], v192 offset:16384
	ds_read_b128 v[210:213], v192 offset:17408
	ds_read_b128 v[216:219], v192 offset:18432
	ds_read_b128 v[220:223], v192 offset:19456
	ds_read_b128 v[224:227], v192 offset:20480
	ds_read_b128 v[228:231], v192 offset:21504
	ds_read_b128 v[244:247], v192 offset:22528
	ds_read_b128 v[248:251], v192 offset:23552
	global_load_lds_dwordx4 v[18:19], off
	v_lshl_add_u64 v[20:21], s[56:57], 0, v[164:165]
	s_mov_b32 m0, s60
	s_addc_u32 vcc_hi, s57, 0
	global_load_lds_dwordx4 v[20:21], off
	v_lshl_add_u64 v[22:23], vcc, 0, v[162:163]
	s_mov_b32 m0, s61
	s_nop 0
	global_load_lds_dwordx4 v[22:23], off
	v_lshl_add_u64 v[22:23], vcc, 0, v[164:165]
	s_mov_b32 m0, s62
	s_nop 0
	global_load_lds_dwordx4 v[22:23], off
	v_cndmask_b32_e64 v22, v195, v193, s[4:5]
	v_lshlrev_b32_e32 v0, 10, v22
	v_and_or_b32 v0, v0, s82, v174
	v_bfe_u32 v22, v22, 16, 16
	s_mov_b32 m0, s65
	v_lshl_add_u32 v22, v22, 10, v175
	global_load_lds_dwordx4 v0, s[58:59]
	s_mov_b32 m0, s63
	v_mov_b32_e32 v23, v1
	global_load_lds_dwordx4 v22, s[58:59]
	s_waitcnt vmcnt(8)
	s_waitcnt lgkmcnt(0)
	v_lshl_add_u64 v[24:25], s[58:59], 0, v[0:1]
	v_lshl_add_u64 v[22:23], s[58:59], 0, v[22:23]
	s_barrier
	s_waitcnt lgkmcnt(0)
	v_mfma_scale_f32_16x16x128_f8f6f4 v[86:89], v[2:9], v[206:213], v[86:89], v234, v235 op_sel_hi:[0,0,0]
	v_mfma_scale_f32_16x16x128_f8f6f4 v[82:85], v[10:17], v[206:213], v[82:85], v234, v235 op_sel_hi:[0,0,0]
	v_mfma_scale_f32_16x16x128_f8f6f4 v[78:81], v[2:9], v[216:223], v[78:81], v234, v235 op_sel_hi:[0,0,0]
	v_mfma_scale_f32_16x16x128_f8f6f4 v[74:77], v[10:17], v[216:223], v[74:77], v234, v235 op_sel_hi:[0,0,0]
	v_mfma_scale_f32_16x16x128_f8f6f4 v[70:73], v[2:9], v[224:231], v[70:73], v234, v235 op_sel_hi:[0,0,0]
	v_mfma_scale_f32_16x16x128_f8f6f4 v[66:69], v[10:17], v[224:231], v[66:69], v234, v235 op_sel_hi:[0,0,0]
	v_mfma_scale_f32_16x16x128_f8f6f4 v[62:65], v[2:9], v[244:251], v[62:65], v234, v235 op_sel_hi:[0,0,0]
	v_mfma_scale_f32_16x16x128_f8f6f4 v[58:61], v[10:17], v[244:251], v[58:61], v234, v235 op_sel_hi:[0,0,0]
	v_mfma_scale_f32_16x16x128_f8f6f4 v[54:57], v[26:33], v[206:213], v[54:57], v234, v235 op_sel_hi:[0,0,0]
	v_mfma_scale_f32_16x16x128_f8f6f4 v[50:53], v[198:205], v[206:213], v[50:53], v234, v235 op_sel_hi:[0,0,0]
	v_mfma_scale_f32_16x16x128_f8f6f4 v[46:49], v[26:33], v[216:223], v[46:49], v234, v235 op_sel_hi:[0,0,0]
	v_mfma_scale_f32_16x16x128_f8f6f4 v[42:45], v[198:205], v[216:223], v[42:45], v234, v235 op_sel_hi:[0,0,0]
	v_mfma_scale_f32_16x16x128_f8f6f4 v[38:41], v[26:33], v[224:231], v[38:41], v234, v235 op_sel_hi:[0,0,0]
	v_mfma_scale_f32_16x16x128_f8f6f4 v[34:37], v[198:205], v[224:231], v[34:37], v234, v235 op_sel_hi:[0,0,0]
	v_mfma_scale_f32_16x16x128_f8f6f4 v[154:157], v[26:33], v[244:251], v[154:157], v234, v235 op_sel_hi:[0,0,0]
	v_mfma_scale_f32_16x16x128_f8f6f4 v[158:161], v[198:205], v[244:251], v[158:161], v234, v235 op_sel_hi:[0,0,0]
	s_barrier
	ds_read_b128 v[10:13], v184
	ds_read_b128 v[14:17], v185
	ds_read_b128 v[26:29], v186
	ds_read_b128 v[30:33], v187
	ds_read_b128 v[2:5], v188
	ds_read_b128 v[6:9], v189
	ds_read_b128 v[198:201], v190
	ds_read_b128 v[202:205], v191
	v_cndmask_b32_e64 v0, v196, v194, s[4:5]
	v_lshlrev_b32_e32 v170, 10, v0
	s_mov_b32 m0, s10
	v_and_or_b32 v170, v170, s82, v174
	v_bfe_u32 v0, v0, 16, 16
	ds_read_b128 v[206:209], v192 offset:32768
	ds_read_b128 v[210:213], v192 offset:33792
	ds_read_b128 v[216:219], v192 offset:34816
	ds_read_b128 v[220:223], v192 offset:35840
	ds_read_b128 v[224:227], v192 offset:36864
	ds_read_b128 v[228:231], v192 offset:37888
	ds_read_b128 v[244:247], v192 offset:38912
	ds_read_b128 v[248:251], v192 offset:39936
	v_lshl_add_u32 v0, v0, 10, v175
	global_load_lds_dwordx4 v170, s[58:59]
	s_mov_b32 m0, s11
	s_nop 0
	global_load_lds_dwordx4 v0, s[58:59]
	s_waitcnt vmcnt(8)
	s_waitcnt lgkmcnt(0)
	s_barrier
	s_waitcnt lgkmcnt(0)
	v_mfma_scale_f32_16x16x128_f8f6f4 v[150:153], v[10:17], v[206:213], v[150:153], v234, v235 op_sel_hi:[0,0,0]
	v_mfma_scale_f32_16x16x128_f8f6f4 v[146:149], v[26:33], v[206:213], v[146:149], v234, v235 op_sel_hi:[0,0,0]
	v_mfma_scale_f32_16x16x128_f8f6f4 v[142:145], v[10:17], v[216:223], v[142:145], v234, v235 op_sel_hi:[0,0,0]
	v_mfma_scale_f32_16x16x128_f8f6f4 v[138:141], v[26:33], v[216:223], v[138:141], v234, v235 op_sel_hi:[0,0,0]
	v_mfma_scale_f32_16x16x128_f8f6f4 v[134:137], v[10:17], v[224:231], v[134:137], v234, v235 op_sel_hi:[0,0,0]
	v_mfma_scale_f32_16x16x128_f8f6f4 v[130:133], v[26:33], v[224:231], v[130:133], v234, v235 op_sel_hi:[0,0,0]
	v_mfma_scale_f32_16x16x128_f8f6f4 v[126:129], v[10:17], v[244:251], v[126:129], v234, v235 op_sel_hi:[0,0,0]
	v_mfma_scale_f32_16x16x128_f8f6f4 v[122:125], v[26:33], v[244:251], v[122:125], v234, v235 op_sel_hi:[0,0,0]
	v_mfma_scale_f32_16x16x128_f8f6f4 v[118:121], v[2:9], v[206:213], v[118:121], v234, v235 op_sel_hi:[0,0,0]
	v_mfma_scale_f32_16x16x128_f8f6f4 v[114:117], v[198:205], v[206:213], v[114:117], v234, v235 op_sel_hi:[0,0,0]
	v_mfma_scale_f32_16x16x128_f8f6f4 v[110:113], v[2:9], v[216:223], v[110:113], v234, v235 op_sel_hi:[0,0,0]
	v_mfma_scale_f32_16x16x128_f8f6f4 v[106:109], v[198:205], v[216:223], v[106:109], v234, v235 op_sel_hi:[0,0,0]
	v_mfma_scale_f32_16x16x128_f8f6f4 v[102:105], v[2:9], v[224:231], v[102:105], v234, v235 op_sel_hi:[0,0,0]
	v_mfma_scale_f32_16x16x128_f8f6f4 v[98:101], v[198:205], v[224:231], v[98:101], v234, v235 op_sel_hi:[0,0,0]
	v_mfma_scale_f32_16x16x128_f8f6f4 v[94:97], v[2:9], v[244:251], v[94:97], v234, v235 op_sel_hi:[0,0,0]
	v_mfma_scale_f32_16x16x128_f8f6f4 v[90:93], v[198:205], v[244:251], v[90:93], v234, v235 op_sel_hi:[0,0,0]
	s_barrier
	s_mov_b32 m0, s64
	v_lshl_add_u64 v[18:19], v[18:19], 0, s[66:67]
	s_add_u32 s4, s56, 0x20080
	ds_read_b128 v[206:209], v192 offset:49152
	ds_read_b128 v[210:213], v192 offset:50176
	ds_read_b128 v[216:219], v192 offset:51200
	ds_read_b128 v[220:223], v192 offset:52224
	ds_read_b128 v[224:227], v192 offset:53248
	ds_read_b128 v[228:231], v192 offset:54272
	ds_read_b128 v[244:247], v192 offset:55296
	ds_read_b128 v[248:251], v192 offset:56320
	global_load_lds_dwordx4 v[18:19], off
	v_lshl_add_u64 v[18:19], v[20:21], 0, s[66:67]
	s_mov_b32 m0, s81
	s_addc_u32 s5, s57, 0
	global_load_lds_dwordx4 v[18:19], off
	v_lshl_add_u64 v[18:19], s[4:5], 0, v[162:163]
	s_mov_b32 m0, s49
	s_nop 0
	global_load_lds_dwordx4 v[18:19], off
	v_lshl_add_u64 v[18:19], s[4:5], 0, v[164:165]
	s_mov_b32 m0, s30
	s_nop 0
	global_load_lds_dwordx4 v[18:19], off
	v_lshl_add_u64 v[18:19], v[24:25], 0, s[66:67]
	s_mov_b32 m0, s6
	s_nop 0
	global_load_lds_dwordx4 v[18:19], off
	v_lshl_add_u64 v[18:19], v[22:23], 0, s[66:67]
	s_mov_b32 m0, s7
	s_nop 0
	global_load_lds_dwordx4 v[18:19], off
	s_waitcnt vmcnt(8)
	s_waitcnt lgkmcnt(0)
	s_barrier
	s_waitcnt lgkmcnt(0)
	v_mfma_scale_f32_16x16x128_f8f6f4 v[86:89], v[10:17], v[206:213], v[86:89], v234, v235 op_sel_hi:[0,0,0]
	v_mfma_scale_f32_16x16x128_f8f6f4 v[82:85], v[26:33], v[206:213], v[82:85], v234, v235 op_sel_hi:[0,0,0]
	v_mfma_scale_f32_16x16x128_f8f6f4 v[78:81], v[10:17], v[216:223], v[78:81], v234, v235 op_sel_hi:[0,0,0]
	v_mfma_scale_f32_16x16x128_f8f6f4 v[74:77], v[26:33], v[216:223], v[74:77], v234, v235 op_sel_hi:[0,0,0]
	v_mfma_scale_f32_16x16x128_f8f6f4 v[70:73], v[10:17], v[224:231], v[70:73], v234, v235 op_sel_hi:[0,0,0]
	v_mfma_scale_f32_16x16x128_f8f6f4 v[66:69], v[26:33], v[224:231], v[66:69], v234, v235 op_sel_hi:[0,0,0]
	v_mfma_scale_f32_16x16x128_f8f6f4 v[62:65], v[10:17], v[244:251], v[62:65], v234, v235 op_sel_hi:[0,0,0]
	v_mfma_scale_f32_16x16x128_f8f6f4 v[58:61], v[26:33], v[244:251], v[58:61], v234, v235 op_sel_hi:[0,0,0]
	v_mfma_scale_f32_16x16x128_f8f6f4 v[54:57], v[2:9], v[206:213], v[54:57], v234, v235 op_sel_hi:[0,0,0]
	v_mfma_scale_f32_16x16x128_f8f6f4 v[50:53], v[198:205], v[206:213], v[50:53], v234, v235 op_sel_hi:[0,0,0]
	v_mfma_scale_f32_16x16x128_f8f6f4 v[46:49], v[2:9], v[216:223], v[46:49], v234, v235 op_sel_hi:[0,0,0]
	v_mfma_scale_f32_16x16x128_f8f6f4 v[42:45], v[198:205], v[216:223], v[42:45], v234, v235 op_sel_hi:[0,0,0]
	v_mfma_scale_f32_16x16x128_f8f6f4 v[38:41], v[2:9], v[224:231], v[38:41], v234, v235 op_sel_hi:[0,0,0]
	v_mfma_scale_f32_16x16x128_f8f6f4 v[34:37], v[198:205], v[224:231], v[34:37], v234, v235 op_sel_hi:[0,0,0]
	v_mfma_scale_f32_16x16x128_f8f6f4 v[154:157], v[2:9], v[244:251], v[154:157], v234, v235 op_sel_hi:[0,0,0]
	v_mfma_scale_f32_16x16x128_f8f6f4 v[158:161], v[198:205], v[244:251], v[158:161], v234, v235 op_sel_hi:[0,0,0]
	s_barrier
	s_add_i32 s74, s74, 2
	s_add_u32 s54, s54, 0x100
	s_addc_u32 s55, s55, 0
	s_add_u32 s43, s43, 0x100
	s_addc_u32 s45, s45, 0
	s_cmp_gt_u32 s74, 5
	s_cbranch_scc1 .LBB0_2005

.Lrw_done_g2_0:
	s_waitcnt lgkmcnt(0)
	s_barrier
	s_waitcnt lgkmcnt(0)
	v_mfma_scale_f32_16x16x128_f8f6f4 v[158:161], v[18:25], v[172:179], 0, v234, v238 op_sel_hi:[0,0,0]
	v_mfma_scale_f32_16x16x128_f8f6f4 v[154:157], v[26:33], v[172:179], 0, v234, v238 op_sel_hi:[0,0,0]
	v_mfma_scale_f32_16x16x128_f8f6f4 v[150:153], v[18:25], v[198:205], 0, v234, v238 op_sel_hi:[0,0,0]
	v_mfma_scale_f32_16x16x128_f8f6f4 v[146:149], v[26:33], v[198:205], 0, v234, v238 op_sel_hi:[0,0,0]
	v_mfma_scale_f32_16x16x128_f8f6f4 v[142:145], v[18:25], v[206:213], 0, v234, v238 op_sel_hi:[0,0,0]
	v_mfma_scale_f32_16x16x128_f8f6f4 v[138:141], v[26:33], v[206:213], 0, v234, v238 op_sel_hi:[0,0,0]
	v_mfma_scale_f32_16x16x128_f8f6f4 v[134:137], v[18:25], v[216:223], 0, v234, v238 op_sel_hi:[0,0,0]
	v_mfma_scale_f32_16x16x128_f8f6f4 v[130:133], v[26:33], v[216:223], 0, v234, v238 op_sel_hi:[0,0,0]
	v_mfma_scale_f32_16x16x128_f8f6f4 v[126:129], v[2:9], v[172:179], 0, v234, v238 op_sel_hi:[0,0,0]
	v_mfma_scale_f32_16x16x128_f8f6f4 v[122:125], v[10:17], v[172:179], 0, v234, v238 op_sel_hi:[0,0,0]
	v_mfma_scale_f32_16x16x128_f8f6f4 v[118:121], v[2:9], v[198:205], 0, v234, v238 op_sel_hi:[0,0,0]
	v_mfma_scale_f32_16x16x128_f8f6f4 v[114:117], v[10:17], v[198:205], 0, v234, v238 op_sel_hi:[0,0,0]
	v_mfma_scale_f32_16x16x128_f8f6f4 v[110:113], v[2:9], v[206:213], 0, v234, v238 op_sel_hi:[0,0,0]
	v_mfma_scale_f32_16x16x128_f8f6f4 v[106:109], v[10:17], v[206:213], 0, v234, v238 op_sel_hi:[0,0,0]
	v_mfma_scale_f32_16x16x128_f8f6f4 v[102:105], v[2:9], v[216:223], 0, v234, v238 op_sel_hi:[0,0,0]
	v_mfma_scale_f32_16x16x128_f8f6f4 v[98:101], v[10:17], v[216:223], 0, v234, v238 op_sel_hi:[0,0,0]
	s_barrier
	v_lshl_add_u64 v[172:173], s[44:45], 0, v[0:1]
	s_mov_b64 s[48:49], 0x100
	s_mov_b32 m0, s41
	v_lshl_add_u64 v[174:175], v[172:173], 0, s[48:49]
	ds_read_b128 v[198:201], v196 offset:16384
	ds_read_b128 v[202:205], v196 offset:17408
	ds_read_b128 v[206:209], v196 offset:18432
	ds_read_b128 v[210:213], v196 offset:19456
	ds_read_b128 v[216:219], v196 offset:20480
	ds_read_b128 v[220:223], v196 offset:21504
	ds_read_b128 v[224:227], v196 offset:22528
	ds_read_b128 v[228:231], v196 offset:23552
	global_load_lds_dwordx4 v[174:175], off
	v_lshl_add_u64 v[174:175], s[44:45], 0, v[166:167]
	s_add_u32 s46, s44, 0x20100
	v_lshl_add_u64 v[176:177], v[174:175], 0, s[48:49]
	s_mov_b32 m0, s57
	s_addc_u32 s47, s45, 0
	global_load_lds_dwordx4 v[176:177], off
	v_lshl_add_u64 v[176:177], s[46:47], 0, v[0:1]
	s_mov_b32 m0, s58
	s_nop 0
	global_load_lds_dwordx4 v[176:177], off
	v_lshl_add_u64 v[176:177], s[46:47], 0, v[166:167]
	s_mov_b32 m0, s59
	s_nop 0
	global_load_lds_dwordx4 v[176:177], off
	v_lshl_add_u64 v[176:177], s[42:43], 0, v[162:163]
	v_lshl_add_u64 v[178:179], v[176:177], 0, s[48:49]
	s_mov_b32 m0, s37
	s_nop 0
	global_load_lds_dwordx4 v[178:179], off
	v_lshl_add_u64 v[178:179], s[42:43], 0, v[164:165]
	v_lshl_add_u64 v[232:233], v[178:179], 0, s[48:49]
	s_mov_b32 m0, s60
	s_nop 0
	global_load_lds_dwordx4 v[232:233], off
	s_cmp_eq_u32 s26, 0
	s_cbranch_scc1 .Lrw_first_g2_1
	s_waitcnt vmcnt(24)
	s_branch .Lrw_done_g2_1

.Lrw_done_g2_1:
	s_waitcnt lgkmcnt(0)
	s_barrier
	s_waitcnt lgkmcnt(0)
	v_mfma_scale_f32_16x16x128_f8f6f4 v[94:97], v[18:25], v[198:205], 0, v234, v238 op_sel_hi:[0,0,0]
	v_mfma_scale_f32_16x16x128_f8f6f4 v[90:93], v[26:33], v[198:205], 0, v234, v238 op_sel_hi:[0,0,0]
	v_mfma_scale_f32_16x16x128_f8f6f4 v[86:89], v[18:25], v[206:213], 0, v234, v238 op_sel_hi:[0,0,0]
	v_mfma_scale_f32_16x16x128_f8f6f4 v[82:85], v[26:33], v[206:213], 0, v234, v238 op_sel_hi:[0,0,0]
	v_mfma_scale_f32_16x16x128_f8f6f4 v[78:81], v[18:25], v[216:223], 0, v234, v238 op_sel_hi:[0,0,0]
	v_mfma_scale_f32_16x16x128_f8f6f4 v[74:77], v[26:33], v[216:223], 0, v234, v238 op_sel_hi:[0,0,0]
	v_mfma_scale_f32_16x16x128_f8f6f4 v[70:73], v[18:25], v[224:231], 0, v234, v238 op_sel_hi:[0,0,0]
	v_mfma_scale_f32_16x16x128_f8f6f4 v[66:69], v[26:33], v[224:231], 0, v234, v238 op_sel_hi:[0,0,0]
	v_mfma_scale_f32_16x16x128_f8f6f4 v[62:65], v[2:9], v[198:205], 0, v234, v238 op_sel_hi:[0,0,0]
	v_mfma_scale_f32_16x16x128_f8f6f4 v[58:61], v[10:17], v[198:205], 0, v234, v238 op_sel_hi:[0,0,0]
	v_mfma_scale_f32_16x16x128_f8f6f4 v[54:57], v[2:9], v[206:213], 0, v234, v238 op_sel_hi:[0,0,0]
	v_mfma_scale_f32_16x16x128_f8f6f4 v[50:53], v[10:17], v[206:213], 0, v234, v238 op_sel_hi:[0,0,0]
	v_mfma_scale_f32_16x16x128_f8f6f4 v[46:49], v[2:9], v[216:223], 0, v234, v238 op_sel_hi:[0,0,0]
	v_mfma_scale_f32_16x16x128_f8f6f4 v[42:45], v[10:17], v[216:223], 0, v234, v238 op_sel_hi:[0,0,0]
	v_mfma_scale_f32_16x16x128_f8f6f4 v[38:41], v[2:9], v[224:231], 0, v234, v238 op_sel_hi:[0,0,0]
	v_mfma_scale_f32_16x16x128_f8f6f4 v[34:37], v[10:17], v[224:231], 0, v234, v238 op_sel_hi:[0,0,0]
	s_barrier
	ds_read_b128 v[18:21], v188
	ds_read_b128 v[22:25], v189
	ds_read_b128 v[26:29], v190
	ds_read_b128 v[30:33], v191
	ds_read_b128 v[2:5], v192
	ds_read_b128 v[6:9], v193
	ds_read_b128 v[10:13], v194
	ds_read_b128 v[14:17], v195
	s_add_u32 s46, s42, 0x20100
	s_addc_u32 s47, s43, 0
	s_mov_b32 m0, s61
	v_lshl_add_u64 v[232:233], s[46:47], 0, v[162:163]
	ds_read_b128 v[198:201], v196 offset:32768
	ds_read_b128 v[202:205], v196 offset:33792
	ds_read_b128 v[206:209], v196 offset:34816
	ds_read_b128 v[210:213], v196 offset:35840
	ds_read_b128 v[216:219], v196 offset:36864
	ds_read_b128 v[220:223], v196 offset:37888
	ds_read_b128 v[224:227], v196 offset:38912
	ds_read_b128 v[228:231], v196 offset:39936
	global_load_lds_dwordx4 v[232:233], off
	v_lshl_add_u64 v[232:233], s[46:47], 0, v[164:165]
	s_mov_b32 m0, s62
	s_nop 0
	global_load_lds_dwordx4 v[232:233], off
	s_waitcnt vmcnt(8)
	s_waitcnt lgkmcnt(0)
	s_barrier
	s_waitcnt lgkmcnt(0)
	v_mfma_scale_f32_16x16x128_f8f6f4 v[158:161], v[18:25], v[198:205], v[158:161], v234, v238 op_sel_hi:[0,0,0]
	v_mfma_scale_f32_16x16x128_f8f6f4 v[154:157], v[26:33], v[198:205], v[154:157], v234, v238 op_sel_hi:[0,0,0]
	v_mfma_scale_f32_16x16x128_f8f6f4 v[150:153], v[18:25], v[206:213], v[150:153], v234, v238 op_sel_hi:[0,0,0]
	v_mfma_scale_f32_16x16x128_f8f6f4 v[146:149], v[26:33], v[206:213], v[146:149], v234, v238 op_sel_hi:[0,0,0]
	v_mfma_scale_f32_16x16x128_f8f6f4 v[142:145], v[18:25], v[216:223], v[142:145], v234, v238 op_sel_hi:[0,0,0]
	v_mfma_scale_f32_16x16x128_f8f6f4 v[138:141], v[26:33], v[216:223], v[138:141], v234, v238 op_sel_hi:[0,0,0]
	v_mfma_scale_f32_16x16x128_f8f6f4 v[134:137], v[18:25], v[224:231], v[134:137], v234, v238 op_sel_hi:[0,0,0]
	v_mfma_scale_f32_16x16x128_f8f6f4 v[130:133], v[26:33], v[224:231], v[130:133], v234, v238 op_sel_hi:[0,0,0]
	v_mfma_scale_f32_16x16x128_f8f6f4 v[126:129], v[2:9], v[198:205], v[126:129], v234, v238 op_sel_hi:[0,0,0]
	v_mfma_scale_f32_16x16x128_f8f6f4 v[122:125], v[10:17], v[198:205], v[122:125], v234, v238 op_sel_hi:[0,0,0]
	v_mfma_scale_f32_16x16x128_f8f6f4 v[118:121], v[2:9], v[206:213], v[118:121], v234, v238 op_sel_hi:[0,0,0]
	v_mfma_scale_f32_16x16x128_f8f6f4 v[114:117], v[10:17], v[206:213], v[114:117], v234, v238 op_sel_hi:[0,0,0]
	v_mfma_scale_f32_16x16x128_f8f6f4 v[110:113], v[2:9], v[216:223], v[110:113], v234, v238 op_sel_hi:[0,0,0]
	v_mfma_scale_f32_16x16x128_f8f6f4 v[106:109], v[10:17], v[216:223], v[106:109], v234, v238 op_sel_hi:[0,0,0]
	v_mfma_scale_f32_16x16x128_f8f6f4 v[102:105], v[2:9], v[224:231], v[102:105], v234, v238 op_sel_hi:[0,0,0]
	v_mfma_scale_f32_16x16x128_f8f6f4 v[98:101], v[10:17], v[224:231], v[98:101], v234, v238 op_sel_hi:[0,0,0]
	s_barrier
	s_mov_b64 s[48:49], 0x180
	s_mov_b32 m0, s65
	v_lshl_add_u64 v[172:173], v[172:173], 0, s[48:49]
	s_add_u32 s46, s44, 0x20180
	ds_read_b128 v[198:201], v196 offset:49152
	ds_read_b128 v[202:205], v196 offset:50176
	ds_read_b128 v[206:209], v196 offset:51200
	ds_read_b128 v[210:213], v196 offset:52224
	ds_read_b128 v[216:219], v196 offset:53248
	ds_read_b128 v[220:223], v196 offset:54272
	ds_read_b128 v[224:227], v196 offset:55296
	ds_read_b128 v[228:231], v196 offset:56320
	global_load_lds_dwordx4 v[172:173], off
	v_lshl_add_u64 v[172:173], v[174:175], 0, s[48:49]
	s_mov_b32 m0, s68
	s_addc_u32 s47, s45, 0
	global_load_lds_dwordx4 v[172:173], off
	v_lshl_add_u64 v[172:173], s[46:47], 0, v[0:1]
	s_mov_b32 m0, s51
	s_nop 0
	global_load_lds_dwordx4 v[172:173], off
	v_lshl_add_u64 v[172:173], s[46:47], 0, v[166:167]
	s_mov_b32 m0, s4
	s_nop 0
	global_load_lds_dwordx4 v[172:173], off
	v_lshl_add_u64 v[172:173], v[176:177], 0, s[48:49]
	s_mov_b32 m0, s81
	s_nop 0
	global_load_lds_dwordx4 v[172:173], off
	v_lshl_add_u64 v[172:173], v[178:179], 0, s[48:49]
	s_mov_b32 m0, s50
	s_nop 0
	global_load_lds_dwordx4 v[172:173], off
	s_waitcnt vmcnt(8)
	s_waitcnt lgkmcnt(0)
	s_barrier
	s_waitcnt lgkmcnt(0)
	v_mfma_scale_f32_16x16x128_f8f6f4 v[94:97], v[18:25], v[198:205], v[94:97], v234, v238 op_sel_hi:[0,0,0]
	v_mfma_scale_f32_16x16x128_f8f6f4 v[90:93], v[26:33], v[198:205], v[90:93], v234, v238 op_sel_hi:[0,0,0]
	v_mfma_scale_f32_16x16x128_f8f6f4 v[86:89], v[18:25], v[206:213], v[86:89], v234, v238 op_sel_hi:[0,0,0]
	v_mfma_scale_f32_16x16x128_f8f6f4 v[82:85], v[26:33], v[206:213], v[82:85], v234, v238 op_sel_hi:[0,0,0]
	v_mfma_scale_f32_16x16x128_f8f6f4 v[78:81], v[18:25], v[216:223], v[78:81], v234, v238 op_sel_hi:[0,0,0]
	v_mfma_scale_f32_16x16x128_f8f6f4 v[74:77], v[26:33], v[216:223], v[74:77], v234, v238 op_sel_hi:[0,0,0]
	v_mfma_scale_f32_16x16x128_f8f6f4 v[70:73], v[18:25], v[224:231], v[70:73], v234, v238 op_sel_hi:[0,0,0]
	v_mfma_scale_f32_16x16x128_f8f6f4 v[66:69], v[26:33], v[224:231], v[66:69], v234, v238 op_sel_hi:[0,0,0]
	v_mfma_scale_f32_16x16x128_f8f6f4 v[62:65], v[2:9], v[198:205], v[62:65], v234, v238 op_sel_hi:[0,0,0]
	v_mfma_scale_f32_16x16x128_f8f6f4 v[58:61], v[10:17], v[198:205], v[58:61], v234, v238 op_sel_hi:[0,0,0]
	v_mfma_scale_f32_16x16x128_f8f6f4 v[54:57], v[2:9], v[206:213], v[54:57], v234, v238 op_sel_hi:[0,0,0]
	v_mfma_scale_f32_16x16x128_f8f6f4 v[50:53], v[10:17], v[206:213], v[50:53], v234, v238 op_sel_hi:[0,0,0]
	v_mfma_scale_f32_16x16x128_f8f6f4 v[46:49], v[2:9], v[216:223], v[46:49], v234, v238 op_sel_hi:[0,0,0]
	v_mfma_scale_f32_16x16x128_f8f6f4 v[42:45], v[10:17], v[216:223], v[42:45], v234, v238 op_sel_hi:[0,0,0]
	v_mfma_scale_f32_16x16x128_f8f6f4 v[38:41], v[2:9], v[224:231], v[38:41], v234, v238 op_sel_hi:[0,0,0]
	v_mfma_scale_f32_16x16x128_f8f6f4 v[34:37], v[10:17], v[224:231], v[34:37], v234, v238 op_sel_hi:[0,0,0]
	s_barrier
	s_add_u32 s42, s42, 0x20180
	s_addc_u32 s43, s43, 0
	s_add_u32 s48, s44, 0x200
	s_addc_u32 s49, s45, 0
	s_mov_b32 s74, 0
.LBB0_2089:
	ds_read_b128 v[2:5], v180
	ds_read_b128 v[6:9], v181
	ds_read_b128 v[10:13], v182
	ds_read_b128 v[14:17], v183
	ds_read_b128 v[26:29], v184
	ds_read_b128 v[30:33], v185
	ds_read_b128 v[172:175], v186
	ds_read_b128 v[176:179], v187
	s_add_u32 s44, s42, 0xfffe0080
	s_addc_u32 s45, s43, -1
	s_cmp_eq_u32 s74, 4
	s_cselect_b32 s47, s13, s45
	s_cselect_b32 s46, s27, s44
	s_cselect_b32 s45, s35, s49
	s_cselect_b32 s44, s34, s48
	s_mov_b32 m0, s29
	v_lshl_add_u64 v[224:225], s[42:43], 0, v[168:169]
	ds_read_b128 v[18:21], v196
	ds_read_b128 v[22:25], v196 offset:1024
	ds_read_b128 v[198:201], v196 offset:2048
	ds_read_b128 v[202:205], v196 offset:3072
	ds_read_b128 v[206:209], v196 offset:4096
	ds_read_b128 v[210:213], v196 offset:5120
	ds_read_b128 v[216:219], v196 offset:6144
	ds_read_b128 v[220:223], v196 offset:7168
	global_load_lds_dwordx4 v[224:225], off
	v_lshl_add_u64 v[224:225], s[42:43], 0, v[170:171]
	s_mov_b32 m0, s31
	s_nop 0
	global_load_lds_dwordx4 v[224:225], off
	s_waitcnt vmcnt(8)
	s_waitcnt lgkmcnt(0)
	s_barrier
	s_waitcnt lgkmcnt(0)
	v_mfma_scale_f32_16x16x128_f8f6f4 v[158:161], v[2:9], v[18:25], v[158:161], v234, v238 op_sel_hi:[0,0,0]
	v_mfma_scale_f32_16x16x128_f8f6f4 v[154:157], v[10:17], v[18:25], v[154:157], v234, v238 op_sel_hi:[0,0,0]
	v_mfma_scale_f32_16x16x128_f8f6f4 v[150:153], v[2:9], v[198:205], v[150:153], v234, v238 op_sel_hi:[0,0,0]
	v_mfma_scale_f32_16x16x128_f8f6f4 v[146:149], v[10:17], v[198:205], v[146:149], v234, v238 op_sel_hi:[0,0,0]
	v_mfma_scale_f32_16x16x128_f8f6f4 v[142:145], v[2:9], v[206:213], v[142:145], v234, v238 op_sel_hi:[0,0,0]
	v_mfma_scale_f32_16x16x128_f8f6f4 v[138:141], v[10:17], v[206:213], v[138:141], v234, v238 op_sel_hi:[0,0,0]
	v_mfma_scale_f32_16x16x128_f8f6f4 v[134:137], v[2:9], v[216:223], v[134:137], v234, v238 op_sel_hi:[0,0,0]
	v_mfma_scale_f32_16x16x128_f8f6f4 v[130:133], v[10:17], v[216:223], v[130:133], v234, v238 op_sel_hi:[0,0,0]
	v_mfma_scale_f32_16x16x128_f8f6f4 v[126:129], v[26:33], v[18:25], v[126:129], v234, v238 op_sel_hi:[0,0,0]
	v_mfma_scale_f32_16x16x128_f8f6f4 v[122:125], v[172:179], v[18:25], v[122:125], v234, v238 op_sel_hi:[0,0,0]
	v_mfma_scale_f32_16x16x128_f8f6f4 v[118:121], v[26:33], v[198:205], v[118:121], v234, v238 op_sel_hi:[0,0,0]
	v_mfma_scale_f32_16x16x128_f8f6f4 v[114:117], v[172:179], v[198:205], v[114:117], v234, v238 op_sel_hi:[0,0,0]
	v_mfma_scale_f32_16x16x128_f8f6f4 v[110:113], v[26:33], v[206:213], v[110:113], v234, v238 op_sel_hi:[0,0,0]
	v_mfma_scale_f32_16x16x128_f8f6f4 v[106:109], v[172:179], v[206:213], v[106:109], v234, v238 op_sel_hi:[0,0,0]
	v_mfma_scale_f32_16x16x128_f8f6f4 v[102:105], v[26:33], v[216:223], v[102:105], v234, v238 op_sel_hi:[0,0,0]
	v_mfma_scale_f32_16x16x128_f8f6f4 v[98:101], v[172:179], v[216:223], v[98:101], v234, v238 op_sel_hi:[0,0,0]
	s_barrier
	s_mov_b32 m0, s41
	v_lshl_add_u64 v[18:19], s[44:45], 0, v[0:1]
	s_add_u32 vcc_lo, s44, 0x20000
	ds_read_b128 v[198:201], v196 offset:16384
	ds_read_b128 v[202:205], v196 offset:17408
	ds_read_b128 v[206:209], v196 offset:18432
	ds_read_b128 v[210:213], v196 offset:19456
	ds_read_b128 v[216:219], v196 offset:20480
	ds_read_b128 v[220:223], v196 offset:21504
	ds_read_b128 v[224:227], v196 offset:22528
	ds_read_b128 v[228:231], v196 offset:23552
	global_load_lds_dwordx4 v[18:19], off
	v_lshl_add_u64 v[20:21], s[44:45], 0, v[166:167]
	s_mov_b32 m0, s57
	s_addc_u32 vcc_hi, s45, 0
	global_load_lds_dwordx4 v[20:21], off
	v_lshl_add_u64 v[22:23], vcc, 0, v[0:1]
	s_mov_b32 m0, s58
	v_lshl_add_u64 v[24:25], s[46:47], 0, v[164:165]
	global_load_lds_dwordx4 v[22:23], off
	v_lshl_add_u64 v[22:23], vcc, 0, v[166:167]
	s_mov_b32 m0, s59
	s_nop 0
	global_load_lds_dwordx4 v[22:23], off
	v_lshl_add_u64 v[22:23], s[46:47], 0, v[162:163]
	s_mov_b32 m0, s37
	s_nop 0
	global_load_lds_dwordx4 v[22:23], off
	s_mov_b32 m0, s60
	s_nop 0
	global_load_lds_dwordx4 v[24:25], off
	s_waitcnt vmcnt(8)
	s_waitcnt lgkmcnt(0)
	s_barrier
	s_waitcnt lgkmcnt(0)
	v_mfma_scale_f32_16x16x128_f8f6f4 v[94:97], v[2:9], v[198:205], v[94:97], v234, v238 op_sel_hi:[0,0,0]
	v_mfma_scale_f32_16x16x128_f8f6f4 v[90:93], v[10:17], v[198:205], v[90:93], v234, v238 op_sel_hi:[0,0,0]
	v_mfma_scale_f32_16x16x128_f8f6f4 v[86:89], v[2:9], v[206:213], v[86:89], v234, v238 op_sel_hi:[0,0,0]
	v_mfma_scale_f32_16x16x128_f8f6f4 v[82:85], v[10:17], v[206:213], v[82:85], v234, v238 op_sel_hi:[0,0,0]
	v_mfma_scale_f32_16x16x128_f8f6f4 v[78:81], v[2:9], v[216:223], v[78:81], v234, v238 op_sel_hi:[0,0,0]
	v_mfma_scale_f32_16x16x128_f8f6f4 v[74:77], v[10:17], v[216:223], v[74:77], v234, v238 op_sel_hi:[0,0,0]
	v_mfma_scale_f32_16x16x128_f8f6f4 v[70:73], v[2:9], v[224:231], v[70:73], v234, v238 op_sel_hi:[0,0,0]
	v_mfma_scale_f32_16x16x128_f8f6f4 v[66:69], v[10:17], v[224:231], v[66:69], v234, v238 op_sel_hi:[0,0,0]
	v_mfma_scale_f32_16x16x128_f8f6f4 v[62:65], v[26:33], v[198:205], v[62:65], v234, v238 op_sel_hi:[0,0,0]
	v_mfma_scale_f32_16x16x128_f8f6f4 v[58:61], v[172:179], v[198:205], v[58:61], v234, v238 op_sel_hi:[0,0,0]
	v_mfma_scale_f32_16x16x128_f8f6f4 v[54:57], v[26:33], v[206:213], v[54:57], v234, v238 op_sel_hi:[0,0,0]
	v_mfma_scale_f32_16x16x128_f8f6f4 v[50:53], v[172:179], v[206:213], v[50:53], v234, v238 op_sel_hi:[0,0,0]
	v_mfma_scale_f32_16x16x128_f8f6f4 v[46:49], v[26:33], v[216:223], v[46:49], v234, v238 op_sel_hi:[0,0,0]
	v_mfma_scale_f32_16x16x128_f8f6f4 v[42:45], v[172:179], v[216:223], v[42:45], v234, v238 op_sel_hi:[0,0,0]
	v_mfma_scale_f32_16x16x128_f8f6f4 v[38:41], v[26:33], v[224:231], v[38:41], v234, v238 op_sel_hi:[0,0,0]
	v_mfma_scale_f32_16x16x128_f8f6f4 v[34:37], v[172:179], v[224:231], v[34:37], v234, v238 op_sel_hi:[0,0,0]
	s_barrier
	ds_read_b128 v[10:13], v188
	ds_read_b128 v[14:17], v189
	ds_read_b128 v[26:29], v190
	ds_read_b128 v[30:33], v191
	ds_read_b128 v[2:5], v192
	ds_read_b128 v[6:9], v193
	ds_read_b128 v[172:175], v194
	ds_read_b128 v[176:179], v195
	s_add_u32 s46, s46, 0x20000
	s_addc_u32 s47, s47, 0
	s_mov_b32 m0, s61
	v_lshl_add_u64 v[232:233], s[46:47], 0, v[162:163]
	ds_read_b128 v[198:201], v196 offset:32768
	ds_read_b128 v[202:205], v196 offset:33792
	ds_read_b128 v[206:209], v196 offset:34816
	ds_read_b128 v[210:213], v196 offset:35840
	ds_read_b128 v[216:219], v196 offset:36864
	ds_read_b128 v[220:223], v196 offset:37888
	ds_read_b128 v[224:227], v196 offset:38912
	ds_read_b128 v[228:231], v196 offset:39936
	global_load_lds_dwordx4 v[232:233], off
	v_lshl_add_u64 v[232:233], s[46:47], 0, v[164:165]
	s_mov_b32 m0, s62
	s_nop 0
	global_load_lds_dwordx4 v[232:233], off
	s_waitcnt vmcnt(8)
	s_waitcnt lgkmcnt(0)
	s_barrier
	s_waitcnt lgkmcnt(0)
	v_mfma_scale_f32_16x16x128_f8f6f4 v[158:161], v[10:17], v[198:205], v[158:161], v234, v238 op_sel_hi:[0,0,0]
	v_mfma_scale_f32_16x16x128_f8f6f4 v[154:157], v[26:33], v[198:205], v[154:157], v234, v238 op_sel_hi:[0,0,0]
	v_mfma_scale_f32_16x16x128_f8f6f4 v[150:153], v[10:17], v[206:213], v[150:153], v234, v238 op_sel_hi:[0,0,0]
	v_mfma_scale_f32_16x16x128_f8f6f4 v[146:149], v[26:33], v[206:213], v[146:149], v234, v238 op_sel_hi:[0,0,0]
	v_mfma_scale_f32_16x16x128_f8f6f4 v[142:145], v[10:17], v[216:223], v[142:145], v234, v238 op_sel_hi:[0,0,0]
	v_mfma_scale_f32_16x16x128_f8f6f4 v[138:141], v[26:33], v[216:223], v[138:141], v234, v238 op_sel_hi:[0,0,0]
	v_mfma_scale_f32_16x16x128_f8f6f4 v[134:137], v[10:17], v[224:231], v[134:137], v234, v238 op_sel_hi:[0,0,0]
	v_mfma_scale_f32_16x16x128_f8f6f4 v[130:133], v[26:33], v[224:231], v[130:133], v234, v238 op_sel_hi:[0,0,0]
	v_mfma_scale_f32_16x16x128_f8f6f4 v[126:129], v[2:9], v[198:205], v[126:129], v234, v238 op_sel_hi:[0,0,0]
	v_mfma_scale_f32_16x16x128_f8f6f4 v[122:125], v[172:179], v[198:205], v[122:125], v234, v238 op_sel_hi:[0,0,0]
	v_mfma_scale_f32_16x16x128_f8f6f4 v[118:121], v[2:9], v[206:213], v[118:121], v234, v238 op_sel_hi:[0,0,0]
	v_mfma_scale_f32_16x16x128_f8f6f4 v[114:117], v[172:179], v[206:213], v[114:117], v234, v238 op_sel_hi:[0,0,0]
	v_mfma_scale_f32_16x16x128_f8f6f4 v[110:113], v[2:9], v[216:223], v[110:113], v234, v238 op_sel_hi:[0,0,0]
	v_mfma_scale_f32_16x16x128_f8f6f4 v[106:109], v[172:179], v[216:223], v[106:109], v234, v238 op_sel_hi:[0,0,0]
	v_mfma_scale_f32_16x16x128_f8f6f4 v[102:105], v[2:9], v[224:231], v[102:105], v234, v238 op_sel_hi:[0,0,0]
	v_mfma_scale_f32_16x16x128_f8f6f4 v[98:101], v[172:179], v[224:231], v[98:101], v234, v238 op_sel_hi:[0,0,0]
	s_barrier
	s_mov_b32 m0, s65
	v_lshl_add_u64 v[18:19], v[18:19], 0, s[66:67]
	s_add_u32 s44, s44, 0x20080
	ds_read_b128 v[198:201], v196 offset:49152
	ds_read_b128 v[202:205], v196 offset:50176
	ds_read_b128 v[206:209], v196 offset:51200
	ds_read_b128 v[210:213], v196 offset:52224
	ds_read_b128 v[216:219], v196 offset:53248
	ds_read_b128 v[220:223], v196 offset:54272
	ds_read_b128 v[224:227], v196 offset:55296
	ds_read_b128 v[228:231], v196 offset:56320
	global_load_lds_dwordx4 v[18:19], off
	v_lshl_add_u64 v[18:19], v[20:21], 0, s[66:67]
	s_mov_b32 m0, s68
	s_addc_u32 s45, s45, 0
	global_load_lds_dwordx4 v[18:19], off
	v_lshl_add_u64 v[18:19], s[44:45], 0, v[0:1]
	s_mov_b32 m0, s51
	s_nop 0
	global_load_lds_dwordx4 v[18:19], off
	v_lshl_add_u64 v[18:19], s[44:45], 0, v[166:167]
	s_mov_b32 m0, s4
	s_nop 0
	global_load_lds_dwordx4 v[18:19], off
	v_lshl_add_u64 v[18:19], v[22:23], 0, s[66:67]
	s_mov_b32 m0, s81
	s_nop 0
	global_load_lds_dwordx4 v[18:19], off
	v_lshl_add_u64 v[18:19], v[24:25], 0, s[66:67]
	s_mov_b32 m0, s50
	s_nop 0
	global_load_lds_dwordx4 v[18:19], off
	s_waitcnt vmcnt(8)
	s_waitcnt lgkmcnt(0)
	s_barrier
	s_waitcnt lgkmcnt(0)
	v_mfma_scale_f32_16x16x128_f8f6f4 v[94:97], v[10:17], v[198:205], v[94:97], v234, v238 op_sel_hi:[0,0,0]
	v_mfma_scale_f32_16x16x128_f8f6f4 v[90:93], v[26:33], v[198:205], v[90:93], v234, v238 op_sel_hi:[0,0,0]
	v_mfma_scale_f32_16x16x128_f8f6f4 v[86:89], v[10:17], v[206:213], v[86:89], v234, v238 op_sel_hi:[0,0,0]
	v_mfma_scale_f32_16x16x128_f8f6f4 v[82:85], v[26:33], v[206:213], v[82:85], v234, v238 op_sel_hi:[0,0,0]
	v_mfma_scale_f32_16x16x128_f8f6f4 v[78:81], v[10:17], v[216:223], v[78:81], v234, v238 op_sel_hi:[0,0,0]
	v_mfma_scale_f32_16x16x128_f8f6f4 v[74:77], v[26:33], v[216:223], v[74:77], v234, v238 op_sel_hi:[0,0,0]
	v_mfma_scale_f32_16x16x128_f8f6f4 v[70:73], v[10:17], v[224:231], v[70:73], v234, v238 op_sel_hi:[0,0,0]
	v_mfma_scale_f32_16x16x128_f8f6f4 v[66:69], v[26:33], v[224:231], v[66:69], v234, v238 op_sel_hi:[0,0,0]
	v_mfma_scale_f32_16x16x128_f8f6f4 v[62:65], v[2:9], v[198:205], v[62:65], v234, v238 op_sel_hi:[0,0,0]
	v_mfma_scale_f32_16x16x128_f8f6f4 v[58:61], v[172:179], v[198:205], v[58:61], v234, v238 op_sel_hi:[0,0,0]
	v_mfma_scale_f32_16x16x128_f8f6f4 v[54:57], v[2:9], v[206:213], v[54:57], v234, v238 op_sel_hi:[0,0,0]
	v_mfma_scale_f32_16x16x128_f8f6f4 v[50:53], v[172:179], v[206:213], v[50:53], v234, v238 op_sel_hi:[0,0,0]
	v_mfma_scale_f32_16x16x128_f8f6f4 v[46:49], v[2:9], v[216:223], v[46:49], v234, v238 op_sel_hi:[0,0,0]
	v_mfma_scale_f32_16x16x128_f8f6f4 v[42:45], v[172:179], v[216:223], v[42:45], v234, v238 op_sel_hi:[0,0,0]
	v_mfma_scale_f32_16x16x128_f8f6f4 v[38:41], v[2:9], v[224:231], v[38:41], v234, v238 op_sel_hi:[0,0,0]
	v_mfma_scale_f32_16x16x128_f8f6f4 v[34:37], v[172:179], v[224:231], v[34:37], v234, v238 op_sel_hi:[0,0,0]
	s_barrier
	s_add_i32 s74, s74, 2
	s_add_u32 s42, s42, 0x100
	s_addc_u32 s43, s43, 0
	s_add_u32 s48, s48, 0x100
	s_addc_u32 s49, s49, 0
	s_cmp_gt_u32 s74, 5
	s_cbranch_scc0 .LBB0_2089
	s_and_b64 vcc, exec, s[8:9]
	s_cbranch_vccz .LBB0_2092
	s_barrier
